# PEER u-side row dots rewritten as software-pipelined packed-f32 FMA chains (fewer VALU ops), 256-VGPR allocation
# speedup vs baseline: 1.0039x; 1.0039x over previous
.LBB0_1473:
	s_or_b64 exec, exec, s[30:31]
	s_mov_b32 s31, 0
	v_readlane_b32 s30, v76, 0
	s_lshl_b32 s30, s30, 12
	v_lshl_add_u64 v[194:195], v[86:87], 0, s[30:31]
	global_load_dwordx4 v[10:13], v[194:195], off
	global_load_dwordx4 v[14:17], v[194:195], off offset:1024
	global_load_dwordx4 v[18:21], v[194:195], off offset:2048
	global_load_dwordx4 v[22:25], v[194:195], off offset:3072
	v_readlane_b32 s30, v76, 1
	s_lshl_b32 s30, s30, 12
	v_lshl_add_u64 v[194:195], v[86:87], 0, s[30:31]
	global_load_dwordx4 v[26:29], v[194:195], off
	global_load_dwordx4 v[30:33], v[194:195], off offset:1024
	global_load_dwordx4 v[34:37], v[194:195], off offset:2048
	global_load_dwordx4 v[38:41], v[194:195], off offset:3072
	v_readlane_b32 s30, v76, 2
	s_lshl_b32 s30, s30, 12
	v_lshl_add_u64 v[194:195], v[86:87], 0, s[30:31]
	global_load_dwordx4 v[42:45], v[194:195], off
	global_load_dwordx4 v[46:49], v[194:195], off offset:1024
	global_load_dwordx4 v[50:53], v[194:195], off offset:2048
	global_load_dwordx4 v[54:57], v[194:195], off offset:3072
	v_readlane_b32 s30, v76, 3
	s_lshl_b32 s30, s30, 12
	v_lshl_add_u64 v[194:195], v[86:87], 0, s[30:31]
	global_load_dwordx4 v[58:61], v[194:195], off
	global_load_dwordx4 v[62:65], v[194:195], off offset:1024
	global_load_dwordx4 v[66:69], v[194:195], off offset:2048
	global_load_dwordx4 v[70:73], v[194:195], off offset:3072
	v_readlane_b32 s30, v76, 4
	s_lshl_b32 s30, s30, 12
	v_lshl_add_u64 v[194:195], v[86:87], 0, s[30:31]
	s_waitcnt vmcnt(15)
	v_cvt_f32_ubyte0_e32 v240, v10
	v_cvt_f32_ubyte1_e32 v241, v10
	v_cvt_f32_ubyte2_e32 v242, v10
	v_cvt_f32_ubyte3_e32 v243, v10
	v_cvt_f32_ubyte0_e32 v244, v11
	v_cvt_f32_ubyte1_e32 v245, v11
	v_cvt_f32_ubyte2_e32 v246, v11
	v_cvt_f32_ubyte3_e32 v247, v11
	v_pk_mul_f32 v[248:249], v[240:241], v[162:163]
	v_pk_mul_f32 v[250:251], v[242:243], v[160:161]
	v_cvt_f32_ubyte0_e32 v240, v12
	v_cvt_f32_ubyte1_e32 v241, v12
	v_cvt_f32_ubyte2_e32 v242, v12
	v_cvt_f32_ubyte3_e32 v243, v12
	v_pk_fma_f32 v[248:249], v[244:245], v[158:159], v[248:249]
	v_pk_fma_f32 v[250:251], v[246:247], v[148:149], v[250:251]
	v_cvt_f32_ubyte0_e32 v244, v13
	v_cvt_f32_ubyte1_e32 v245, v13
	v_cvt_f32_ubyte2_e32 v246, v13
	v_cvt_f32_ubyte3_e32 v247, v13
	global_load_dwordx4 v[10:13], v[194:195], off
	v_pk_fma_f32 v[248:249], v[240:241], v[140:141], v[248:249]
	v_pk_fma_f32 v[250:251], v[242:243], v[128:129], v[250:251]
	s_waitcnt vmcnt(15)
	v_cvt_f32_ubyte0_e32 v240, v14
	v_cvt_f32_ubyte1_e32 v241, v14
	v_cvt_f32_ubyte2_e32 v242, v14
	v_cvt_f32_ubyte3_e32 v243, v14
	v_pk_fma_f32 v[248:249], v[244:245], v[120:121], v[248:249]
	v_pk_fma_f32 v[250:251], v[246:247], v[112:113], v[250:251]
	v_cvt_f32_ubyte0_e32 v244, v15
	v_cvt_f32_ubyte1_e32 v245, v15
	v_cvt_f32_ubyte2_e32 v246, v15
	v_cvt_f32_ubyte3_e32 v247, v15
	v_pk_fma_f32 v[248:249], v[240:241], v[106:107], v[248:249]
	v_pk_fma_f32 v[250:251], v[242:243], v[102:103], v[250:251]
	v_cvt_f32_ubyte0_e32 v240, v16
	v_cvt_f32_ubyte1_e32 v241, v16
	v_cvt_f32_ubyte2_e32 v242, v16
	v_cvt_f32_ubyte3_e32 v243, v16
	v_pk_fma_f32 v[248:249], v[244:245], v[152:153], v[248:249]
	v_pk_fma_f32 v[250:251], v[246:247], v[100:101], v[250:251]
	v_cvt_f32_ubyte0_e32 v244, v17
	v_cvt_f32_ubyte1_e32 v245, v17
	v_cvt_f32_ubyte2_e32 v246, v17
	v_cvt_f32_ubyte3_e32 v247, v17
	global_load_dwordx4 v[14:17], v[194:195], off offset:1024
	v_pk_fma_f32 v[248:249], v[240:241], v[136:137], v[248:249]
	v_pk_fma_f32 v[250:251], v[242:243], v[122:123], v[250:251]
	s_waitcnt vmcnt(15)
	v_cvt_f32_ubyte0_e32 v240, v18
	v_cvt_f32_ubyte1_e32 v241, v18
	v_cvt_f32_ubyte2_e32 v242, v18
	v_cvt_f32_ubyte3_e32 v243, v18
	v_pk_fma_f32 v[248:249], v[244:245], v[116:117], v[248:249]
	v_pk_fma_f32 v[250:251], v[246:247], v[110:111], v[250:251]
	v_cvt_f32_ubyte0_e32 v244, v19
	v_cvt_f32_ubyte1_e32 v245, v19
	v_cvt_f32_ubyte2_e32 v246, v19
	v_cvt_f32_ubyte3_e32 v247, v19
	v_pk_fma_f32 v[248:249], v[240:241], v[156:157], v[248:249]
	v_pk_fma_f32 v[250:251], v[242:243], v[146:147], v[250:251]
	v_cvt_f32_ubyte0_e32 v240, v20
	v_cvt_f32_ubyte1_e32 v241, v20
	v_cvt_f32_ubyte2_e32 v242, v20
	v_cvt_f32_ubyte3_e32 v243, v20
	v_pk_fma_f32 v[248:249], v[244:245], v[142:143], v[248:249]
	v_pk_fma_f32 v[250:251], v[246:247], v[130:131], v[250:251]
	v_cvt_f32_ubyte0_e32 v244, v21
	v_cvt_f32_ubyte1_e32 v245, v21
	v_cvt_f32_ubyte2_e32 v246, v21
	v_cvt_f32_ubyte3_e32 v247, v21
	global_load_dwordx4 v[18:21], v[194:195], off offset:2048
	v_pk_fma_f32 v[248:249], v[240:241], v[124:125], v[248:249]
	v_pk_fma_f32 v[250:251], v[242:243], v[114:115], v[250:251]
	s_waitcnt vmcnt(15)
	v_cvt_f32_ubyte0_e32 v240, v22
	v_cvt_f32_ubyte1_e32 v241, v22
	v_cvt_f32_ubyte2_e32 v242, v22
	v_cvt_f32_ubyte3_e32 v243, v22
	v_pk_fma_f32 v[248:249], v[244:245], v[108:109], v[248:249]
	v_pk_fma_f32 v[250:251], v[246:247], v[104:105], v[250:251]
	v_cvt_f32_ubyte0_e32 v244, v23
	v_cvt_f32_ubyte1_e32 v245, v23
	v_cvt_f32_ubyte2_e32 v246, v23
	v_cvt_f32_ubyte3_e32 v247, v23
	v_pk_fma_f32 v[248:249], v[240:241], v[154:155], v[248:249]
	v_pk_fma_f32 v[250:251], v[242:243], v[138:139], v[250:251]
	v_cvt_f32_ubyte0_e32 v240, v24
	v_cvt_f32_ubyte1_e32 v241, v24
	v_cvt_f32_ubyte2_e32 v242, v24
	v_cvt_f32_ubyte3_e32 v243, v24
	v_pk_fma_f32 v[248:249], v[244:245], v[150:151], v[248:249]
	v_pk_fma_f32 v[250:251], v[246:247], v[132:133], v[250:251]
	v_cvt_f32_ubyte0_e32 v244, v25
	v_cvt_f32_ubyte1_e32 v245, v25
	v_cvt_f32_ubyte2_e32 v246, v25
	v_cvt_f32_ubyte3_e32 v247, v25
	global_load_dwordx4 v[22:25], v[194:195], off offset:3072
	v_pk_fma_f32 v[248:249], v[240:241], v[144:145], v[248:249]
	v_pk_fma_f32 v[250:251], v[242:243], v[126:127], v[250:251]
	v_readlane_b32 s30, v76, 5
	s_lshl_b32 s30, s30, 12
	v_lshl_add_u64 v[194:195], v[86:87], 0, s[30:31]
	s_waitcnt vmcnt(15)
	v_cvt_f32_ubyte0_e32 v240, v26
	v_cvt_f32_ubyte1_e32 v241, v26
	v_cvt_f32_ubyte2_e32 v242, v26
	v_cvt_f32_ubyte3_e32 v243, v26
	v_pk_fma_f32 v[248:249], v[244:245], v[134:135], v[248:249]
	v_pk_fma_f32 v[250:251], v[246:247], v[118:119], v[250:251]
	v_cvt_f32_ubyte0_e32 v244, v27
	v_cvt_f32_ubyte1_e32 v245, v27
	v_cvt_f32_ubyte2_e32 v246, v27
	v_cvt_f32_ubyte3_e32 v247, v27
	v_pk_add_f32 v[252:253], v[248:249], v[250:251]
	v_pk_mul_f32 v[248:249], v[240:241], v[162:163]
	v_pk_mul_f32 v[250:251], v[242:243], v[160:161]
	v_cvt_f32_ubyte0_e32 v240, v28
	v_cvt_f32_ubyte1_e32 v241, v28
	v_cvt_f32_ubyte2_e32 v242, v28
	v_cvt_f32_ubyte3_e32 v243, v28
	v_pk_fma_f32 v[248:249], v[244:245], v[158:159], v[248:249]
	v_pk_fma_f32 v[250:251], v[246:247], v[148:149], v[250:251]
	v_add_f32_e32 v178, v252, v253
	v_cvt_f32_ubyte0_e32 v244, v29
	v_cvt_f32_ubyte1_e32 v245, v29
	v_cvt_f32_ubyte2_e32 v246, v29
	v_cvt_f32_ubyte3_e32 v247, v29
	global_load_dwordx4 v[26:29], v[194:195], off
	v_pk_fma_f32 v[248:249], v[240:241], v[140:141], v[248:249]
	v_pk_fma_f32 v[250:251], v[242:243], v[128:129], v[250:251]
	s_waitcnt vmcnt(15)
	v_cvt_f32_ubyte0_e32 v240, v30
	v_cvt_f32_ubyte1_e32 v241, v30
	v_cvt_f32_ubyte2_e32 v242, v30
	v_cvt_f32_ubyte3_e32 v243, v30
	v_pk_fma_f32 v[248:249], v[244:245], v[120:121], v[248:249]
	v_pk_fma_f32 v[250:251], v[246:247], v[112:113], v[250:251]
	v_cvt_f32_ubyte0_e32 v244, v31
	v_cvt_f32_ubyte1_e32 v245, v31
	v_cvt_f32_ubyte2_e32 v246, v31
	v_cvt_f32_ubyte3_e32 v247, v31
	v_pk_fma_f32 v[248:249], v[240:241], v[106:107], v[248:249]
	v_pk_fma_f32 v[250:251], v[242:243], v[102:103], v[250:251]
	v_cvt_f32_ubyte0_e32 v240, v32
	v_cvt_f32_ubyte1_e32 v241, v32
	v_cvt_f32_ubyte2_e32 v242, v32
	v_cvt_f32_ubyte3_e32 v243, v32
	v_pk_fma_f32 v[248:249], v[244:245], v[152:153], v[248:249]
	v_pk_fma_f32 v[250:251], v[246:247], v[100:101], v[250:251]
	v_cvt_f32_ubyte0_e32 v244, v33
	v_cvt_f32_ubyte1_e32 v245, v33
	v_cvt_f32_ubyte2_e32 v246, v33
	v_cvt_f32_ubyte3_e32 v247, v33
	global_load_dwordx4 v[30:33], v[194:195], off offset:1024
	v_pk_fma_f32 v[248:249], v[240:241], v[136:137], v[248:249]
	v_pk_fma_f32 v[250:251], v[242:243], v[122:123], v[250:251]
	s_waitcnt vmcnt(15)
	v_cvt_f32_ubyte0_e32 v240, v34
	v_cvt_f32_ubyte1_e32 v241, v34
	v_cvt_f32_ubyte2_e32 v242, v34
	v_cvt_f32_ubyte3_e32 v243, v34
	v_pk_fma_f32 v[248:249], v[244:245], v[116:117], v[248:249]
	v_pk_fma_f32 v[250:251], v[246:247], v[110:111], v[250:251]
	v_cvt_f32_ubyte0_e32 v244, v35
	v_cvt_f32_ubyte1_e32 v245, v35
	v_cvt_f32_ubyte2_e32 v246, v35
	v_cvt_f32_ubyte3_e32 v247, v35
	v_pk_fma_f32 v[248:249], v[240:241], v[156:157], v[248:249]
	v_pk_fma_f32 v[250:251], v[242:243], v[146:147], v[250:251]
	v_cvt_f32_ubyte0_e32 v240, v36
	v_cvt_f32_ubyte1_e32 v241, v36
	v_cvt_f32_ubyte2_e32 v242, v36
	v_cvt_f32_ubyte3_e32 v243, v36
	v_pk_fma_f32 v[248:249], v[244:245], v[142:143], v[248:249]
	v_pk_fma_f32 v[250:251], v[246:247], v[130:131], v[250:251]
	v_cvt_f32_ubyte0_e32 v244, v37
	v_cvt_f32_ubyte1_e32 v245, v37
	v_cvt_f32_ubyte2_e32 v246, v37
	v_cvt_f32_ubyte3_e32 v247, v37
	global_load_dwordx4 v[34:37], v[194:195], off offset:2048
	v_pk_fma_f32 v[248:249], v[240:241], v[124:125], v[248:249]
	v_pk_fma_f32 v[250:251], v[242:243], v[114:115], v[250:251]
	s_waitcnt vmcnt(15)
	v_cvt_f32_ubyte0_e32 v240, v38
	v_cvt_f32_ubyte1_e32 v241, v38
	v_cvt_f32_ubyte2_e32 v242, v38
	v_cvt_f32_ubyte3_e32 v243, v38
	v_pk_fma_f32 v[248:249], v[244:245], v[108:109], v[248:249]
	v_pk_fma_f32 v[250:251], v[246:247], v[104:105], v[250:251]
	v_cvt_f32_ubyte0_e32 v244, v39
	v_cvt_f32_ubyte1_e32 v245, v39
	v_cvt_f32_ubyte2_e32 v246, v39
	v_cvt_f32_ubyte3_e32 v247, v39
	v_pk_fma_f32 v[248:249], v[240:241], v[154:155], v[248:249]
	v_pk_fma_f32 v[250:251], v[242:243], v[138:139], v[250:251]
	v_cvt_f32_ubyte0_e32 v240, v40
	v_cvt_f32_ubyte1_e32 v241, v40
	v_cvt_f32_ubyte2_e32 v242, v40
	v_cvt_f32_ubyte3_e32 v243, v40
	v_pk_fma_f32 v[248:249], v[244:245], v[150:151], v[248:249]
	v_pk_fma_f32 v[250:251], v[246:247], v[132:133], v[250:251]
	v_cvt_f32_ubyte0_e32 v244, v41
	v_cvt_f32_ubyte1_e32 v245, v41
	v_cvt_f32_ubyte2_e32 v246, v41
	v_cvt_f32_ubyte3_e32 v247, v41
	global_load_dwordx4 v[38:41], v[194:195], off offset:3072
	v_pk_fma_f32 v[248:249], v[240:241], v[144:145], v[248:249]
	v_pk_fma_f32 v[250:251], v[242:243], v[126:127], v[250:251]
	v_readlane_b32 s30, v76, 6
	s_lshl_b32 s30, s30, 12
	v_lshl_add_u64 v[194:195], v[86:87], 0, s[30:31]
	s_waitcnt vmcnt(15)
	v_cvt_f32_ubyte0_e32 v240, v42
	v_cvt_f32_ubyte1_e32 v241, v42
	v_cvt_f32_ubyte2_e32 v242, v42
	v_cvt_f32_ubyte3_e32 v243, v42
	v_pk_fma_f32 v[248:249], v[244:245], v[134:135], v[248:249]
	v_pk_fma_f32 v[250:251], v[246:247], v[118:119], v[250:251]
	v_cvt_f32_ubyte0_e32 v244, v43
	v_cvt_f32_ubyte1_e32 v245, v43
	v_cvt_f32_ubyte2_e32 v246, v43
	v_cvt_f32_ubyte3_e32 v247, v43
	v_pk_add_f32 v[252:253], v[248:249], v[250:251]
	v_pk_mul_f32 v[248:249], v[240:241], v[162:163]
	v_pk_mul_f32 v[250:251], v[242:243], v[160:161]
	v_cvt_f32_ubyte0_e32 v240, v44
	v_cvt_f32_ubyte1_e32 v241, v44
	v_cvt_f32_ubyte2_e32 v242, v44
	v_cvt_f32_ubyte3_e32 v243, v44
	v_pk_fma_f32 v[248:249], v[244:245], v[158:159], v[248:249]
	v_pk_fma_f32 v[250:251], v[246:247], v[148:149], v[250:251]
	v_add_f32_e32 v179, v252, v253
	v_cvt_f32_ubyte0_e32 v244, v45
	v_cvt_f32_ubyte1_e32 v245, v45
	v_cvt_f32_ubyte2_e32 v246, v45
	v_cvt_f32_ubyte3_e32 v247, v45
	global_load_dwordx4 v[42:45], v[194:195], off
	v_pk_fma_f32 v[248:249], v[240:241], v[140:141], v[248:249]
	v_pk_fma_f32 v[250:251], v[242:243], v[128:129], v[250:251]
	s_waitcnt vmcnt(15)
	v_cvt_f32_ubyte0_e32 v240, v46
	v_cvt_f32_ubyte1_e32 v241, v46
	v_cvt_f32_ubyte2_e32 v242, v46
	v_cvt_f32_ubyte3_e32 v243, v46
	v_pk_fma_f32 v[248:249], v[244:245], v[120:121], v[248:249]
	v_pk_fma_f32 v[250:251], v[246:247], v[112:113], v[250:251]
	v_cvt_f32_ubyte0_e32 v244, v47
	v_cvt_f32_ubyte1_e32 v245, v47
	v_cvt_f32_ubyte2_e32 v246, v47
	v_cvt_f32_ubyte3_e32 v247, v47
	v_pk_fma_f32 v[248:249], v[240:241], v[106:107], v[248:249]
	v_pk_fma_f32 v[250:251], v[242:243], v[102:103], v[250:251]
	v_cvt_f32_ubyte0_e32 v240, v48
	v_cvt_f32_ubyte1_e32 v241, v48
	v_cvt_f32_ubyte2_e32 v242, v48
	v_cvt_f32_ubyte3_e32 v243, v48
	v_pk_fma_f32 v[248:249], v[244:245], v[152:153], v[248:249]
	v_pk_fma_f32 v[250:251], v[246:247], v[100:101], v[250:251]
	v_cvt_f32_ubyte0_e32 v244, v49
	v_cvt_f32_ubyte1_e32 v245, v49
	v_cvt_f32_ubyte2_e32 v246, v49
	v_cvt_f32_ubyte3_e32 v247, v49
	global_load_dwordx4 v[46:49], v[194:195], off offset:1024
	v_pk_fma_f32 v[248:249], v[240:241], v[136:137], v[248:249]
	v_pk_fma_f32 v[250:251], v[242:243], v[122:123], v[250:251]
	s_waitcnt vmcnt(15)
	v_cvt_f32_ubyte0_e32 v240, v50
	v_cvt_f32_ubyte1_e32 v241, v50
	v_cvt_f32_ubyte2_e32 v242, v50
	v_cvt_f32_ubyte3_e32 v243, v50
	v_pk_fma_f32 v[248:249], v[244:245], v[116:117], v[248:249]
	v_pk_fma_f32 v[250:251], v[246:247], v[110:111], v[250:251]
	v_cvt_f32_ubyte0_e32 v244, v51
	v_cvt_f32_ubyte1_e32 v245, v51
	v_cvt_f32_ubyte2_e32 v246, v51
	v_cvt_f32_ubyte3_e32 v247, v51
	v_pk_fma_f32 v[248:249], v[240:241], v[156:157], v[248:249]
	v_pk_fma_f32 v[250:251], v[242:243], v[146:147], v[250:251]
	v_cvt_f32_ubyte0_e32 v240, v52
	v_cvt_f32_ubyte1_e32 v241, v52
	v_cvt_f32_ubyte2_e32 v242, v52
	v_cvt_f32_ubyte3_e32 v243, v52
	v_pk_fma_f32 v[248:249], v[244:245], v[142:143], v[248:249]
	v_pk_fma_f32 v[250:251], v[246:247], v[130:131], v[250:251]
	v_cvt_f32_ubyte0_e32 v244, v53
	v_cvt_f32_ubyte1_e32 v245, v53
	v_cvt_f32_ubyte2_e32 v246, v53
	v_cvt_f32_ubyte3_e32 v247, v53
	global_load_dwordx4 v[50:53], v[194:195], off offset:2048
	v_pk_fma_f32 v[248:249], v[240:241], v[124:125], v[248:249]
	v_pk_fma_f32 v[250:251], v[242:243], v[114:115], v[250:251]
	s_waitcnt vmcnt(15)
	v_cvt_f32_ubyte0_e32 v240, v54
	v_cvt_f32_ubyte1_e32 v241, v54
	v_cvt_f32_ubyte2_e32 v242, v54
	v_cvt_f32_ubyte3_e32 v243, v54
	v_pk_fma_f32 v[248:249], v[244:245], v[108:109], v[248:249]
	v_pk_fma_f32 v[250:251], v[246:247], v[104:105], v[250:251]
	v_cvt_f32_ubyte0_e32 v244, v55
	v_cvt_f32_ubyte1_e32 v245, v55
	v_cvt_f32_ubyte2_e32 v246, v55
	v_cvt_f32_ubyte3_e32 v247, v55
	v_pk_fma_f32 v[248:249], v[240:241], v[154:155], v[248:249]
	v_pk_fma_f32 v[250:251], v[242:243], v[138:139], v[250:251]
	v_cvt_f32_ubyte0_e32 v240, v56
	v_cvt_f32_ubyte1_e32 v241, v56
	v_cvt_f32_ubyte2_e32 v242, v56
	v_cvt_f32_ubyte3_e32 v243, v56
	v_pk_fma_f32 v[248:249], v[244:245], v[150:151], v[248:249]
	v_pk_fma_f32 v[250:251], v[246:247], v[132:133], v[250:251]
	v_cvt_f32_ubyte0_e32 v244, v57
	v_cvt_f32_ubyte1_e32 v245, v57
	v_cvt_f32_ubyte2_e32 v246, v57
	v_cvt_f32_ubyte3_e32 v247, v57
	global_load_dwordx4 v[54:57], v[194:195], off offset:3072
	v_pk_fma_f32 v[248:249], v[240:241], v[144:145], v[248:249]
	v_pk_fma_f32 v[250:251], v[242:243], v[126:127], v[250:251]
	v_readlane_b32 s30, v76, 7
	s_lshl_b32 s30, s30, 12
	v_lshl_add_u64 v[194:195], v[86:87], 0, s[30:31]
	s_waitcnt vmcnt(15)
	v_cvt_f32_ubyte0_e32 v240, v58
	v_cvt_f32_ubyte1_e32 v241, v58
	v_cvt_f32_ubyte2_e32 v242, v58
	v_cvt_f32_ubyte3_e32 v243, v58
	v_pk_fma_f32 v[248:249], v[244:245], v[134:135], v[248:249]
	v_pk_fma_f32 v[250:251], v[246:247], v[118:119], v[250:251]
	v_cvt_f32_ubyte0_e32 v244, v59
	v_cvt_f32_ubyte1_e32 v245, v59
	v_cvt_f32_ubyte2_e32 v246, v59
	v_cvt_f32_ubyte3_e32 v247, v59
	v_pk_add_f32 v[252:253], v[248:249], v[250:251]
	v_pk_mul_f32 v[248:249], v[240:241], v[162:163]
	v_pk_mul_f32 v[250:251], v[242:243], v[160:161]
	v_cvt_f32_ubyte0_e32 v240, v60
	v_cvt_f32_ubyte1_e32 v241, v60
	v_cvt_f32_ubyte2_e32 v242, v60
	v_cvt_f32_ubyte3_e32 v243, v60
	v_pk_fma_f32 v[248:249], v[244:245], v[158:159], v[248:249]
	v_pk_fma_f32 v[250:251], v[246:247], v[148:149], v[250:251]
	v_add_f32_e32 v180, v252, v253
	v_cvt_f32_ubyte0_e32 v244, v61
	v_cvt_f32_ubyte1_e32 v245, v61
	v_cvt_f32_ubyte2_e32 v246, v61
	v_cvt_f32_ubyte3_e32 v247, v61
	global_load_dwordx4 v[58:61], v[194:195], off
	v_pk_fma_f32 v[248:249], v[240:241], v[140:141], v[248:249]
	v_pk_fma_f32 v[250:251], v[242:243], v[128:129], v[250:251]
	s_waitcnt vmcnt(15)
	v_cvt_f32_ubyte0_e32 v240, v62
	v_cvt_f32_ubyte1_e32 v241, v62
	v_cvt_f32_ubyte2_e32 v242, v62
	v_cvt_f32_ubyte3_e32 v243, v62
	v_pk_fma_f32 v[248:249], v[244:245], v[120:121], v[248:249]
	v_pk_fma_f32 v[250:251], v[246:247], v[112:113], v[250:251]
	v_cvt_f32_ubyte0_e32 v244, v63
	v_cvt_f32_ubyte1_e32 v245, v63
	v_cvt_f32_ubyte2_e32 v246, v63
	v_cvt_f32_ubyte3_e32 v247, v63
	v_pk_fma_f32 v[248:249], v[240:241], v[106:107], v[248:249]
	v_pk_fma_f32 v[250:251], v[242:243], v[102:103], v[250:251]
	v_cvt_f32_ubyte0_e32 v240, v64
	v_cvt_f32_ubyte1_e32 v241, v64
	v_cvt_f32_ubyte2_e32 v242, v64
	v_cvt_f32_ubyte3_e32 v243, v64
	v_pk_fma_f32 v[248:249], v[244:245], v[152:153], v[248:249]
	v_pk_fma_f32 v[250:251], v[246:247], v[100:101], v[250:251]
	v_cvt_f32_ubyte0_e32 v244, v65
	v_cvt_f32_ubyte1_e32 v245, v65
	v_cvt_f32_ubyte2_e32 v246, v65
	v_cvt_f32_ubyte3_e32 v247, v65
	global_load_dwordx4 v[62:65], v[194:195], off offset:1024
	v_pk_fma_f32 v[248:249], v[240:241], v[136:137], v[248:249]
	v_pk_fma_f32 v[250:251], v[242:243], v[122:123], v[250:251]
	s_waitcnt vmcnt(15)
	v_cvt_f32_ubyte0_e32 v240, v66
	v_cvt_f32_ubyte1_e32 v241, v66
	v_cvt_f32_ubyte2_e32 v242, v66
	v_cvt_f32_ubyte3_e32 v243, v66
	v_pk_fma_f32 v[248:249], v[244:245], v[116:117], v[248:249]
	v_pk_fma_f32 v[250:251], v[246:247], v[110:111], v[250:251]
	v_cvt_f32_ubyte0_e32 v244, v67
	v_cvt_f32_ubyte1_e32 v245, v67
	v_cvt_f32_ubyte2_e32 v246, v67
	v_cvt_f32_ubyte3_e32 v247, v67
	v_pk_fma_f32 v[248:249], v[240:241], v[156:157], v[248:249]
	v_pk_fma_f32 v[250:251], v[242:243], v[146:147], v[250:251]
	v_cvt_f32_ubyte0_e32 v240, v68
	v_cvt_f32_ubyte1_e32 v241, v68
	v_cvt_f32_ubyte2_e32 v242, v68
	v_cvt_f32_ubyte3_e32 v243, v68
	v_pk_fma_f32 v[248:249], v[244:245], v[142:143], v[248:249]
	v_pk_fma_f32 v[250:251], v[246:247], v[130:131], v[250:251]
	v_cvt_f32_ubyte0_e32 v244, v69
	v_cvt_f32_ubyte1_e32 v245, v69
	v_cvt_f32_ubyte2_e32 v246, v69
	v_cvt_f32_ubyte3_e32 v247, v69
	global_load_dwordx4 v[66:69], v[194:195], off offset:2048
	v_pk_fma_f32 v[248:249], v[240:241], v[124:125], v[248:249]
	v_pk_fma_f32 v[250:251], v[242:243], v[114:115], v[250:251]
	s_waitcnt vmcnt(15)
	v_cvt_f32_ubyte0_e32 v240, v70
	v_cvt_f32_ubyte1_e32 v241, v70
	v_cvt_f32_ubyte2_e32 v242, v70
	v_cvt_f32_ubyte3_e32 v243, v70
	v_pk_fma_f32 v[248:249], v[244:245], v[108:109], v[248:249]
	v_pk_fma_f32 v[250:251], v[246:247], v[104:105], v[250:251]
	v_cvt_f32_ubyte0_e32 v244, v71
	v_cvt_f32_ubyte1_e32 v245, v71
	v_cvt_f32_ubyte2_e32 v246, v71
	v_cvt_f32_ubyte3_e32 v247, v71
	v_pk_fma_f32 v[248:249], v[240:241], v[154:155], v[248:249]
	v_pk_fma_f32 v[250:251], v[242:243], v[138:139], v[250:251]
	v_cvt_f32_ubyte0_e32 v240, v72
	v_cvt_f32_ubyte1_e32 v241, v72
	v_cvt_f32_ubyte2_e32 v242, v72
	v_cvt_f32_ubyte3_e32 v243, v72
	v_pk_fma_f32 v[248:249], v[244:245], v[150:151], v[248:249]
	v_pk_fma_f32 v[250:251], v[246:247], v[132:133], v[250:251]
	v_cvt_f32_ubyte0_e32 v244, v73
	v_cvt_f32_ubyte1_e32 v245, v73
	v_cvt_f32_ubyte2_e32 v246, v73
	v_cvt_f32_ubyte3_e32 v247, v73
	global_load_dwordx4 v[70:73], v[194:195], off offset:3072
	v_pk_fma_f32 v[248:249], v[240:241], v[144:145], v[248:249]
	v_pk_fma_f32 v[250:251], v[242:243], v[126:127], v[250:251]
	v_readlane_b32 s30, v76, 8
	s_lshl_b32 s30, s30, 12
	v_lshl_add_u64 v[194:195], v[86:87], 0, s[30:31]
	s_waitcnt vmcnt(15)
	v_cvt_f32_ubyte0_e32 v240, v10
	v_cvt_f32_ubyte1_e32 v241, v10
	v_cvt_f32_ubyte2_e32 v242, v10
	v_cvt_f32_ubyte3_e32 v243, v10
	v_pk_fma_f32 v[248:249], v[244:245], v[134:135], v[248:249]
	v_pk_fma_f32 v[250:251], v[246:247], v[118:119], v[250:251]
	v_cvt_f32_ubyte0_e32 v244, v11
	v_cvt_f32_ubyte1_e32 v245, v11
	v_cvt_f32_ubyte2_e32 v246, v11
	v_cvt_f32_ubyte3_e32 v247, v11
	v_pk_add_f32 v[252:253], v[248:249], v[250:251]
	v_pk_mul_f32 v[248:249], v[240:241], v[162:163]
	v_pk_mul_f32 v[250:251], v[242:243], v[160:161]
	v_cvt_f32_ubyte0_e32 v240, v12
	v_cvt_f32_ubyte1_e32 v241, v12
	v_cvt_f32_ubyte2_e32 v242, v12
	v_cvt_f32_ubyte3_e32 v243, v12
	v_pk_fma_f32 v[248:249], v[244:245], v[158:159], v[248:249]
	v_pk_fma_f32 v[250:251], v[246:247], v[148:149], v[250:251]
	v_add_f32_e32 v181, v252, v253
	v_cvt_f32_ubyte0_e32 v244, v13
	v_cvt_f32_ubyte1_e32 v245, v13
	v_cvt_f32_ubyte2_e32 v246, v13
	v_cvt_f32_ubyte3_e32 v247, v13
	global_load_dwordx4 v[10:13], v[194:195], off
	v_pk_fma_f32 v[248:249], v[240:241], v[140:141], v[248:249]
	v_pk_fma_f32 v[250:251], v[242:243], v[128:129], v[250:251]
	s_waitcnt vmcnt(15)
	v_cvt_f32_ubyte0_e32 v240, v14
	v_cvt_f32_ubyte1_e32 v241, v14
	v_cvt_f32_ubyte2_e32 v242, v14
	v_cvt_f32_ubyte3_e32 v243, v14
	v_pk_fma_f32 v[248:249], v[244:245], v[120:121], v[248:249]
	v_pk_fma_f32 v[250:251], v[246:247], v[112:113], v[250:251]
	v_cvt_f32_ubyte0_e32 v244, v15
	v_cvt_f32_ubyte1_e32 v245, v15
	v_cvt_f32_ubyte2_e32 v246, v15
	v_cvt_f32_ubyte3_e32 v247, v15
	v_pk_fma_f32 v[248:249], v[240:241], v[106:107], v[248:249]
	v_pk_fma_f32 v[250:251], v[242:243], v[102:103], v[250:251]
	v_cvt_f32_ubyte0_e32 v240, v16
	v_cvt_f32_ubyte1_e32 v241, v16
	v_cvt_f32_ubyte2_e32 v242, v16
	v_cvt_f32_ubyte3_e32 v243, v16
	v_pk_fma_f32 v[248:249], v[244:245], v[152:153], v[248:249]
	v_pk_fma_f32 v[250:251], v[246:247], v[100:101], v[250:251]
	v_cvt_f32_ubyte0_e32 v244, v17
	v_cvt_f32_ubyte1_e32 v245, v17
	v_cvt_f32_ubyte2_e32 v246, v17
	v_cvt_f32_ubyte3_e32 v247, v17
	global_load_dwordx4 v[14:17], v[194:195], off offset:1024
	v_pk_fma_f32 v[248:249], v[240:241], v[136:137], v[248:249]
	v_pk_fma_f32 v[250:251], v[242:243], v[122:123], v[250:251]
	s_waitcnt vmcnt(15)
	v_cvt_f32_ubyte0_e32 v240, v18
	v_cvt_f32_ubyte1_e32 v241, v18
	v_cvt_f32_ubyte2_e32 v242, v18
	v_cvt_f32_ubyte3_e32 v243, v18
	v_pk_fma_f32 v[248:249], v[244:245], v[116:117], v[248:249]
	v_pk_fma_f32 v[250:251], v[246:247], v[110:111], v[250:251]
	v_cvt_f32_ubyte0_e32 v244, v19
	v_cvt_f32_ubyte1_e32 v245, v19
	v_cvt_f32_ubyte2_e32 v246, v19
	v_cvt_f32_ubyte3_e32 v247, v19
	v_pk_fma_f32 v[248:249], v[240:241], v[156:157], v[248:249]
	v_pk_fma_f32 v[250:251], v[242:243], v[146:147], v[250:251]
	v_cvt_f32_ubyte0_e32 v240, v20
	v_cvt_f32_ubyte1_e32 v241, v20
	v_cvt_f32_ubyte2_e32 v242, v20
	v_cvt_f32_ubyte3_e32 v243, v20
	v_pk_fma_f32 v[248:249], v[244:245], v[142:143], v[248:249]
	v_pk_fma_f32 v[250:251], v[246:247], v[130:131], v[250:251]
	v_cvt_f32_ubyte0_e32 v244, v21
	v_cvt_f32_ubyte1_e32 v245, v21
	v_cvt_f32_ubyte2_e32 v246, v21
	v_cvt_f32_ubyte3_e32 v247, v21
	global_load_dwordx4 v[18:21], v[194:195], off offset:2048
	v_pk_fma_f32 v[248:249], v[240:241], v[124:125], v[248:249]
	v_pk_fma_f32 v[250:251], v[242:243], v[114:115], v[250:251]
	s_waitcnt vmcnt(15)
	v_cvt_f32_ubyte0_e32 v240, v22
	v_cvt_f32_ubyte1_e32 v241, v22
	v_cvt_f32_ubyte2_e32 v242, v22
	v_cvt_f32_ubyte3_e32 v243, v22
	v_pk_fma_f32 v[248:249], v[244:245], v[108:109], v[248:249]
	v_pk_fma_f32 v[250:251], v[246:247], v[104:105], v[250:251]
	v_cvt_f32_ubyte0_e32 v244, v23
	v_cvt_f32_ubyte1_e32 v245, v23
	v_cvt_f32_ubyte2_e32 v246, v23
	v_cvt_f32_ubyte3_e32 v247, v23
	v_pk_fma_f32 v[248:249], v[240:241], v[154:155], v[248:249]
	v_pk_fma_f32 v[250:251], v[242:243], v[138:139], v[250:251]
	v_cvt_f32_ubyte0_e32 v240, v24
	v_cvt_f32_ubyte1_e32 v241, v24
	v_cvt_f32_ubyte2_e32 v242, v24
	v_cvt_f32_ubyte3_e32 v243, v24
	v_pk_fma_f32 v[248:249], v[244:245], v[150:151], v[248:249]
	v_pk_fma_f32 v[250:251], v[246:247], v[132:133], v[250:251]
	v_cvt_f32_ubyte0_e32 v244, v25
	v_cvt_f32_ubyte1_e32 v245, v25
	v_cvt_f32_ubyte2_e32 v246, v25
	v_cvt_f32_ubyte3_e32 v247, v25
	global_load_dwordx4 v[22:25], v[194:195], off offset:3072
	v_pk_fma_f32 v[248:249], v[240:241], v[144:145], v[248:249]
	v_pk_fma_f32 v[250:251], v[242:243], v[126:127], v[250:251]
	v_readlane_b32 s30, v76, 9
	s_lshl_b32 s30, s30, 12
	v_lshl_add_u64 v[194:195], v[86:87], 0, s[30:31]
	s_waitcnt vmcnt(15)
	v_cvt_f32_ubyte0_e32 v240, v26
	v_cvt_f32_ubyte1_e32 v241, v26
	v_cvt_f32_ubyte2_e32 v242, v26
	v_cvt_f32_ubyte3_e32 v243, v26
	v_pk_fma_f32 v[248:249], v[244:245], v[134:135], v[248:249]
	v_pk_fma_f32 v[250:251], v[246:247], v[118:119], v[250:251]
	v_cvt_f32_ubyte0_e32 v244, v27
	v_cvt_f32_ubyte1_e32 v245, v27
	v_cvt_f32_ubyte2_e32 v246, v27
	v_cvt_f32_ubyte3_e32 v247, v27
	v_pk_add_f32 v[252:253], v[248:249], v[250:251]
	v_pk_mul_f32 v[248:249], v[240:241], v[162:163]
	v_pk_mul_f32 v[250:251], v[242:243], v[160:161]
	v_cvt_f32_ubyte0_e32 v240, v28
	v_cvt_f32_ubyte1_e32 v241, v28
	v_cvt_f32_ubyte2_e32 v242, v28
	v_cvt_f32_ubyte3_e32 v243, v28
	v_pk_fma_f32 v[248:249], v[244:245], v[158:159], v[248:249]
	v_pk_fma_f32 v[250:251], v[246:247], v[148:149], v[250:251]
	v_add_f32_e32 v182, v252, v253
	v_cvt_f32_ubyte0_e32 v244, v29
	v_cvt_f32_ubyte1_e32 v245, v29
	v_cvt_f32_ubyte2_e32 v246, v29
	v_cvt_f32_ubyte3_e32 v247, v29
	global_load_dwordx4 v[26:29], v[194:195], off
	v_pk_fma_f32 v[248:249], v[240:241], v[140:141], v[248:249]
	v_pk_fma_f32 v[250:251], v[242:243], v[128:129], v[250:251]
	s_waitcnt vmcnt(15)
	v_cvt_f32_ubyte0_e32 v240, v30
	v_cvt_f32_ubyte1_e32 v241, v30
	v_cvt_f32_ubyte2_e32 v242, v30
	v_cvt_f32_ubyte3_e32 v243, v30
	v_pk_fma_f32 v[248:249], v[244:245], v[120:121], v[248:249]
	v_pk_fma_f32 v[250:251], v[246:247], v[112:113], v[250:251]
	v_cvt_f32_ubyte0_e32 v244, v31
	v_cvt_f32_ubyte1_e32 v245, v31
	v_cvt_f32_ubyte2_e32 v246, v31
	v_cvt_f32_ubyte3_e32 v247, v31
	v_pk_fma_f32 v[248:249], v[240:241], v[106:107], v[248:249]
	v_pk_fma_f32 v[250:251], v[242:243], v[102:103], v[250:251]
	v_cvt_f32_ubyte0_e32 v240, v32
	v_cvt_f32_ubyte1_e32 v241, v32
	v_cvt_f32_ubyte2_e32 v242, v32
	v_cvt_f32_ubyte3_e32 v243, v32
	v_pk_fma_f32 v[248:249], v[244:245], v[152:153], v[248:249]
	v_pk_fma_f32 v[250:251], v[246:247], v[100:101], v[250:251]
	v_cvt_f32_ubyte0_e32 v244, v33
	v_cvt_f32_ubyte1_e32 v245, v33
	v_cvt_f32_ubyte2_e32 v246, v33
	v_cvt_f32_ubyte3_e32 v247, v33
	global_load_dwordx4 v[30:33], v[194:195], off offset:1024
	v_pk_fma_f32 v[248:249], v[240:241], v[136:137], v[248:249]
	v_pk_fma_f32 v[250:251], v[242:243], v[122:123], v[250:251]
	s_waitcnt vmcnt(15)
	v_cvt_f32_ubyte0_e32 v240, v34
	v_cvt_f32_ubyte1_e32 v241, v34
	v_cvt_f32_ubyte2_e32 v242, v34
	v_cvt_f32_ubyte3_e32 v243, v34
	v_pk_fma_f32 v[248:249], v[244:245], v[116:117], v[248:249]
	v_pk_fma_f32 v[250:251], v[246:247], v[110:111], v[250:251]
	v_cvt_f32_ubyte0_e32 v244, v35
	v_cvt_f32_ubyte1_e32 v245, v35
	v_cvt_f32_ubyte2_e32 v246, v35
	v_cvt_f32_ubyte3_e32 v247, v35
	v_pk_fma_f32 v[248:249], v[240:241], v[156:157], v[248:249]
	v_pk_fma_f32 v[250:251], v[242:243], v[146:147], v[250:251]
	v_cvt_f32_ubyte0_e32 v240, v36
	v_cvt_f32_ubyte1_e32 v241, v36
	v_cvt_f32_ubyte2_e32 v242, v36
	v_cvt_f32_ubyte3_e32 v243, v36
	v_pk_fma_f32 v[248:249], v[244:245], v[142:143], v[248:249]
	v_pk_fma_f32 v[250:251], v[246:247], v[130:131], v[250:251]
	v_cvt_f32_ubyte0_e32 v244, v37
	v_cvt_f32_ubyte1_e32 v245, v37
	v_cvt_f32_ubyte2_e32 v246, v37
	v_cvt_f32_ubyte3_e32 v247, v37
	global_load_dwordx4 v[34:37], v[194:195], off offset:2048
	v_pk_fma_f32 v[248:249], v[240:241], v[124:125], v[248:249]
	v_pk_fma_f32 v[250:251], v[242:243], v[114:115], v[250:251]
	s_waitcnt vmcnt(15)
	v_cvt_f32_ubyte0_e32 v240, v38
	v_cvt_f32_ubyte1_e32 v241, v38
	v_cvt_f32_ubyte2_e32 v242, v38
	v_cvt_f32_ubyte3_e32 v243, v38
	v_pk_fma_f32 v[248:249], v[244:245], v[108:109], v[248:249]
	v_pk_fma_f32 v[250:251], v[246:247], v[104:105], v[250:251]
	v_cvt_f32_ubyte0_e32 v244, v39
	v_cvt_f32_ubyte1_e32 v245, v39
	v_cvt_f32_ubyte2_e32 v246, v39
	v_cvt_f32_ubyte3_e32 v247, v39
	v_pk_fma_f32 v[248:249], v[240:241], v[154:155], v[248:249]
	v_pk_fma_f32 v[250:251], v[242:243], v[138:139], v[250:251]
	v_cvt_f32_ubyte0_e32 v240, v40
	v_cvt_f32_ubyte1_e32 v241, v40
	v_cvt_f32_ubyte2_e32 v242, v40
	v_cvt_f32_ubyte3_e32 v243, v40
	v_pk_fma_f32 v[248:249], v[244:245], v[150:151], v[248:249]
	v_pk_fma_f32 v[250:251], v[246:247], v[132:133], v[250:251]
	v_cvt_f32_ubyte0_e32 v244, v41
	v_cvt_f32_ubyte1_e32 v245, v41
	v_cvt_f32_ubyte2_e32 v246, v41
	v_cvt_f32_ubyte3_e32 v247, v41
	global_load_dwordx4 v[38:41], v[194:195], off offset:3072
	v_pk_fma_f32 v[248:249], v[240:241], v[144:145], v[248:249]
	v_pk_fma_f32 v[250:251], v[242:243], v[126:127], v[250:251]
	v_readlane_b32 s30, v76, 10
	s_lshl_b32 s30, s30, 12
	v_lshl_add_u64 v[194:195], v[86:87], 0, s[30:31]
	s_waitcnt vmcnt(15)
	v_cvt_f32_ubyte0_e32 v240, v42
	v_cvt_f32_ubyte1_e32 v241, v42
	v_cvt_f32_ubyte2_e32 v242, v42
	v_cvt_f32_ubyte3_e32 v243, v42
	v_pk_fma_f32 v[248:249], v[244:245], v[134:135], v[248:249]
	v_pk_fma_f32 v[250:251], v[246:247], v[118:119], v[250:251]
	v_cvt_f32_ubyte0_e32 v244, v43
	v_cvt_f32_ubyte1_e32 v245, v43
	v_cvt_f32_ubyte2_e32 v246, v43
	v_cvt_f32_ubyte3_e32 v247, v43
	v_pk_add_f32 v[252:253], v[248:249], v[250:251]
	v_pk_mul_f32 v[248:249], v[240:241], v[162:163]
	v_pk_mul_f32 v[250:251], v[242:243], v[160:161]
	v_cvt_f32_ubyte0_e32 v240, v44
	v_cvt_f32_ubyte1_e32 v241, v44
	v_cvt_f32_ubyte2_e32 v242, v44
	v_cvt_f32_ubyte3_e32 v243, v44
	v_pk_fma_f32 v[248:249], v[244:245], v[158:159], v[248:249]
	v_pk_fma_f32 v[250:251], v[246:247], v[148:149], v[250:251]
	v_add_f32_e32 v183, v252, v253
	v_cvt_f32_ubyte0_e32 v244, v45
	v_cvt_f32_ubyte1_e32 v245, v45
	v_cvt_f32_ubyte2_e32 v246, v45
	v_cvt_f32_ubyte3_e32 v247, v45
	global_load_dwordx4 v[42:45], v[194:195], off
	v_pk_fma_f32 v[248:249], v[240:241], v[140:141], v[248:249]
	v_pk_fma_f32 v[250:251], v[242:243], v[128:129], v[250:251]
	s_waitcnt vmcnt(15)
	v_cvt_f32_ubyte0_e32 v240, v46
	v_cvt_f32_ubyte1_e32 v241, v46
	v_cvt_f32_ubyte2_e32 v242, v46
	v_cvt_f32_ubyte3_e32 v243, v46
	v_pk_fma_f32 v[248:249], v[244:245], v[120:121], v[248:249]
	v_pk_fma_f32 v[250:251], v[246:247], v[112:113], v[250:251]
	v_cvt_f32_ubyte0_e32 v244, v47
	v_cvt_f32_ubyte1_e32 v245, v47
	v_cvt_f32_ubyte2_e32 v246, v47
	v_cvt_f32_ubyte3_e32 v247, v47
	v_pk_fma_f32 v[248:249], v[240:241], v[106:107], v[248:249]
	v_pk_fma_f32 v[250:251], v[242:243], v[102:103], v[250:251]
	v_cvt_f32_ubyte0_e32 v240, v48
	v_cvt_f32_ubyte1_e32 v241, v48
	v_cvt_f32_ubyte2_e32 v242, v48
	v_cvt_f32_ubyte3_e32 v243, v48
	v_pk_fma_f32 v[248:249], v[244:245], v[152:153], v[248:249]
	v_pk_fma_f32 v[250:251], v[246:247], v[100:101], v[250:251]
	v_cvt_f32_ubyte0_e32 v244, v49
	v_cvt_f32_ubyte1_e32 v245, v49
	v_cvt_f32_ubyte2_e32 v246, v49
	v_cvt_f32_ubyte3_e32 v247, v49
	global_load_dwordx4 v[46:49], v[194:195], off offset:1024
	v_pk_fma_f32 v[248:249], v[240:241], v[136:137], v[248:249]
	v_pk_fma_f32 v[250:251], v[242:243], v[122:123], v[250:251]
	s_waitcnt vmcnt(15)
	v_cvt_f32_ubyte0_e32 v240, v50
	v_cvt_f32_ubyte1_e32 v241, v50
	v_cvt_f32_ubyte2_e32 v242, v50
	v_cvt_f32_ubyte3_e32 v243, v50
	v_pk_fma_f32 v[248:249], v[244:245], v[116:117], v[248:249]
	v_pk_fma_f32 v[250:251], v[246:247], v[110:111], v[250:251]
	v_cvt_f32_ubyte0_e32 v244, v51
	v_cvt_f32_ubyte1_e32 v245, v51
	v_cvt_f32_ubyte2_e32 v246, v51
	v_cvt_f32_ubyte3_e32 v247, v51
	v_pk_fma_f32 v[248:249], v[240:241], v[156:157], v[248:249]
	v_pk_fma_f32 v[250:251], v[242:243], v[146:147], v[250:251]
	v_cvt_f32_ubyte0_e32 v240, v52
	v_cvt_f32_ubyte1_e32 v241, v52
	v_cvt_f32_ubyte2_e32 v242, v52
	v_cvt_f32_ubyte3_e32 v243, v52
	v_pk_fma_f32 v[248:249], v[244:245], v[142:143], v[248:249]
	v_pk_fma_f32 v[250:251], v[246:247], v[130:131], v[250:251]
	v_cvt_f32_ubyte0_e32 v244, v53
	v_cvt_f32_ubyte1_e32 v245, v53
	v_cvt_f32_ubyte2_e32 v246, v53
	v_cvt_f32_ubyte3_e32 v247, v53
	global_load_dwordx4 v[50:53], v[194:195], off offset:2048
	v_pk_fma_f32 v[248:249], v[240:241], v[124:125], v[248:249]
	v_pk_fma_f32 v[250:251], v[242:243], v[114:115], v[250:251]
	s_waitcnt vmcnt(15)
	v_cvt_f32_ubyte0_e32 v240, v54
	v_cvt_f32_ubyte1_e32 v241, v54
	v_cvt_f32_ubyte2_e32 v242, v54
	v_cvt_f32_ubyte3_e32 v243, v54
	v_pk_fma_f32 v[248:249], v[244:245], v[108:109], v[248:249]
	v_pk_fma_f32 v[250:251], v[246:247], v[104:105], v[250:251]
	v_cvt_f32_ubyte0_e32 v244, v55
	v_cvt_f32_ubyte1_e32 v245, v55
	v_cvt_f32_ubyte2_e32 v246, v55
	v_cvt_f32_ubyte3_e32 v247, v55
	v_pk_fma_f32 v[248:249], v[240:241], v[154:155], v[248:249]
	v_pk_fma_f32 v[250:251], v[242:243], v[138:139], v[250:251]
	v_cvt_f32_ubyte0_e32 v240, v56
	v_cvt_f32_ubyte1_e32 v241, v56
	v_cvt_f32_ubyte2_e32 v242, v56
	v_cvt_f32_ubyte3_e32 v243, v56
	v_pk_fma_f32 v[248:249], v[244:245], v[150:151], v[248:249]
	v_pk_fma_f32 v[250:251], v[246:247], v[132:133], v[250:251]
	v_cvt_f32_ubyte0_e32 v244, v57
	v_cvt_f32_ubyte1_e32 v245, v57
	v_cvt_f32_ubyte2_e32 v246, v57
	v_cvt_f32_ubyte3_e32 v247, v57
	global_load_dwordx4 v[54:57], v[194:195], off offset:3072
	v_pk_fma_f32 v[248:249], v[240:241], v[144:145], v[248:249]
	v_pk_fma_f32 v[250:251], v[242:243], v[126:127], v[250:251]
	v_readlane_b32 s30, v76, 11
	s_lshl_b32 s30, s30, 12
	v_lshl_add_u64 v[194:195], v[86:87], 0, s[30:31]
	s_waitcnt vmcnt(15)
	v_cvt_f32_ubyte0_e32 v240, v58
	v_cvt_f32_ubyte1_e32 v241, v58
	v_cvt_f32_ubyte2_e32 v242, v58
	v_cvt_f32_ubyte3_e32 v243, v58
	v_pk_fma_f32 v[248:249], v[244:245], v[134:135], v[248:249]
	v_pk_fma_f32 v[250:251], v[246:247], v[118:119], v[250:251]
	v_cvt_f32_ubyte0_e32 v244, v59
	v_cvt_f32_ubyte1_e32 v245, v59
	v_cvt_f32_ubyte2_e32 v246, v59
	v_cvt_f32_ubyte3_e32 v247, v59
	v_pk_add_f32 v[252:253], v[248:249], v[250:251]
	v_pk_mul_f32 v[248:249], v[240:241], v[162:163]
	v_pk_mul_f32 v[250:251], v[242:243], v[160:161]
	v_cvt_f32_ubyte0_e32 v240, v60
	v_cvt_f32_ubyte1_e32 v241, v60
	v_cvt_f32_ubyte2_e32 v242, v60
	v_cvt_f32_ubyte3_e32 v243, v60
	v_pk_fma_f32 v[248:249], v[244:245], v[158:159], v[248:249]
	v_pk_fma_f32 v[250:251], v[246:247], v[148:149], v[250:251]
	v_add_f32_e32 v184, v252, v253
	v_cvt_f32_ubyte0_e32 v244, v61
	v_cvt_f32_ubyte1_e32 v245, v61
	v_cvt_f32_ubyte2_e32 v246, v61
	v_cvt_f32_ubyte3_e32 v247, v61
	global_load_dwordx4 v[58:61], v[194:195], off
	v_pk_fma_f32 v[248:249], v[240:241], v[140:141], v[248:249]
	v_pk_fma_f32 v[250:251], v[242:243], v[128:129], v[250:251]
	s_waitcnt vmcnt(15)
	v_cvt_f32_ubyte0_e32 v240, v62
	v_cvt_f32_ubyte1_e32 v241, v62
	v_cvt_f32_ubyte2_e32 v242, v62
	v_cvt_f32_ubyte3_e32 v243, v62
	v_pk_fma_f32 v[248:249], v[244:245], v[120:121], v[248:249]
	v_pk_fma_f32 v[250:251], v[246:247], v[112:113], v[250:251]
	v_cvt_f32_ubyte0_e32 v244, v63
	v_cvt_f32_ubyte1_e32 v245, v63
	v_cvt_f32_ubyte2_e32 v246, v63
	v_cvt_f32_ubyte3_e32 v247, v63
	v_pk_fma_f32 v[248:249], v[240:241], v[106:107], v[248:249]
	v_pk_fma_f32 v[250:251], v[242:243], v[102:103], v[250:251]
	v_cvt_f32_ubyte0_e32 v240, v64
	v_cvt_f32_ubyte1_e32 v241, v64
	v_cvt_f32_ubyte2_e32 v242, v64
	v_cvt_f32_ubyte3_e32 v243, v64
	v_pk_fma_f32 v[248:249], v[244:245], v[152:153], v[248:249]
	v_pk_fma_f32 v[250:251], v[246:247], v[100:101], v[250:251]
	v_cvt_f32_ubyte0_e32 v244, v65
	v_cvt_f32_ubyte1_e32 v245, v65
	v_cvt_f32_ubyte2_e32 v246, v65
	v_cvt_f32_ubyte3_e32 v247, v65
	global_load_dwordx4 v[62:65], v[194:195], off offset:1024
	v_pk_fma_f32 v[248:249], v[240:241], v[136:137], v[248:249]
	v_pk_fma_f32 v[250:251], v[242:243], v[122:123], v[250:251]
	s_waitcnt vmcnt(15)
	v_cvt_f32_ubyte0_e32 v240, v66
	v_cvt_f32_ubyte1_e32 v241, v66
	v_cvt_f32_ubyte2_e32 v242, v66
	v_cvt_f32_ubyte3_e32 v243, v66
	v_pk_fma_f32 v[248:249], v[244:245], v[116:117], v[248:249]
	v_pk_fma_f32 v[250:251], v[246:247], v[110:111], v[250:251]
	v_cvt_f32_ubyte0_e32 v244, v67
	v_cvt_f32_ubyte1_e32 v245, v67
	v_cvt_f32_ubyte2_e32 v246, v67
	v_cvt_f32_ubyte3_e32 v247, v67
	v_pk_fma_f32 v[248:249], v[240:241], v[156:157], v[248:249]
	v_pk_fma_f32 v[250:251], v[242:243], v[146:147], v[250:251]
	v_cvt_f32_ubyte0_e32 v240, v68
	v_cvt_f32_ubyte1_e32 v241, v68
	v_cvt_f32_ubyte2_e32 v242, v68
	v_cvt_f32_ubyte3_e32 v243, v68
	v_pk_fma_f32 v[248:249], v[244:245], v[142:143], v[248:249]
	v_pk_fma_f32 v[250:251], v[246:247], v[130:131], v[250:251]
	v_cvt_f32_ubyte0_e32 v244, v69
	v_cvt_f32_ubyte1_e32 v245, v69
	v_cvt_f32_ubyte2_e32 v246, v69
	v_cvt_f32_ubyte3_e32 v247, v69
	global_load_dwordx4 v[66:69], v[194:195], off offset:2048
	v_pk_fma_f32 v[248:249], v[240:241], v[124:125], v[248:249]
	v_pk_fma_f32 v[250:251], v[242:243], v[114:115], v[250:251]
	s_waitcnt vmcnt(15)
	v_cvt_f32_ubyte0_e32 v240, v70
	v_cvt_f32_ubyte1_e32 v241, v70
	v_cvt_f32_ubyte2_e32 v242, v70
	v_cvt_f32_ubyte3_e32 v243, v70
	v_pk_fma_f32 v[248:249], v[244:245], v[108:109], v[248:249]
	v_pk_fma_f32 v[250:251], v[246:247], v[104:105], v[250:251]
	v_cvt_f32_ubyte0_e32 v244, v71
	v_cvt_f32_ubyte1_e32 v245, v71
	v_cvt_f32_ubyte2_e32 v246, v71
	v_cvt_f32_ubyte3_e32 v247, v71
	v_pk_fma_f32 v[248:249], v[240:241], v[154:155], v[248:249]
	v_pk_fma_f32 v[250:251], v[242:243], v[138:139], v[250:251]
	v_cvt_f32_ubyte0_e32 v240, v72
	v_cvt_f32_ubyte1_e32 v241, v72
	v_cvt_f32_ubyte2_e32 v242, v72
	v_cvt_f32_ubyte3_e32 v243, v72
	v_pk_fma_f32 v[248:249], v[244:245], v[150:151], v[248:249]
	v_pk_fma_f32 v[250:251], v[246:247], v[132:133], v[250:251]
	v_cvt_f32_ubyte0_e32 v244, v73
	v_cvt_f32_ubyte1_e32 v245, v73
	v_cvt_f32_ubyte2_e32 v246, v73
	v_cvt_f32_ubyte3_e32 v247, v73
	global_load_dwordx4 v[70:73], v[194:195], off offset:3072
	v_pk_fma_f32 v[248:249], v[240:241], v[144:145], v[248:249]
	v_pk_fma_f32 v[250:251], v[242:243], v[126:127], v[250:251]
	v_readlane_b32 s30, v76, 12
	s_lshl_b32 s30, s30, 12
	v_lshl_add_u64 v[194:195], v[86:87], 0, s[30:31]
	s_waitcnt vmcnt(15)
	v_cvt_f32_ubyte0_e32 v240, v10
	v_cvt_f32_ubyte1_e32 v241, v10
	v_cvt_f32_ubyte2_e32 v242, v10
	v_cvt_f32_ubyte3_e32 v243, v10
	v_pk_fma_f32 v[248:249], v[244:245], v[134:135], v[248:249]
	v_pk_fma_f32 v[250:251], v[246:247], v[118:119], v[250:251]
	v_cvt_f32_ubyte0_e32 v244, v11
	v_cvt_f32_ubyte1_e32 v245, v11
	v_cvt_f32_ubyte2_e32 v246, v11
	v_cvt_f32_ubyte3_e32 v247, v11
	v_pk_add_f32 v[252:253], v[248:249], v[250:251]
	v_pk_mul_f32 v[248:249], v[240:241], v[162:163]
	v_pk_mul_f32 v[250:251], v[242:243], v[160:161]
	v_cvt_f32_ubyte0_e32 v240, v12
	v_cvt_f32_ubyte1_e32 v241, v12
	v_cvt_f32_ubyte2_e32 v242, v12
	v_cvt_f32_ubyte3_e32 v243, v12
	v_pk_fma_f32 v[248:249], v[244:245], v[158:159], v[248:249]
	v_pk_fma_f32 v[250:251], v[246:247], v[148:149], v[250:251]
	v_add_f32_e32 v185, v252, v253
	v_cvt_f32_ubyte0_e32 v244, v13
	v_cvt_f32_ubyte1_e32 v245, v13
	v_cvt_f32_ubyte2_e32 v246, v13
	v_cvt_f32_ubyte3_e32 v247, v13
	global_load_dwordx4 v[10:13], v[194:195], off
	v_pk_fma_f32 v[248:249], v[240:241], v[140:141], v[248:249]
	v_pk_fma_f32 v[250:251], v[242:243], v[128:129], v[250:251]
	s_waitcnt vmcnt(15)
	v_cvt_f32_ubyte0_e32 v240, v14
	v_cvt_f32_ubyte1_e32 v241, v14
	v_cvt_f32_ubyte2_e32 v242, v14
	v_cvt_f32_ubyte3_e32 v243, v14
	v_pk_fma_f32 v[248:249], v[244:245], v[120:121], v[248:249]
	v_pk_fma_f32 v[250:251], v[246:247], v[112:113], v[250:251]
	v_cvt_f32_ubyte0_e32 v244, v15
	v_cvt_f32_ubyte1_e32 v245, v15
	v_cvt_f32_ubyte2_e32 v246, v15
	v_cvt_f32_ubyte3_e32 v247, v15
	v_pk_fma_f32 v[248:249], v[240:241], v[106:107], v[248:249]
	v_pk_fma_f32 v[250:251], v[242:243], v[102:103], v[250:251]
	v_cvt_f32_ubyte0_e32 v240, v16
	v_cvt_f32_ubyte1_e32 v241, v16
	v_cvt_f32_ubyte2_e32 v242, v16
	v_cvt_f32_ubyte3_e32 v243, v16
	v_pk_fma_f32 v[248:249], v[244:245], v[152:153], v[248:249]
	v_pk_fma_f32 v[250:251], v[246:247], v[100:101], v[250:251]
	v_cvt_f32_ubyte0_e32 v244, v17
	v_cvt_f32_ubyte1_e32 v245, v17
	v_cvt_f32_ubyte2_e32 v246, v17
	v_cvt_f32_ubyte3_e32 v247, v17
	global_load_dwordx4 v[14:17], v[194:195], off offset:1024
	v_pk_fma_f32 v[248:249], v[240:241], v[136:137], v[248:249]
	v_pk_fma_f32 v[250:251], v[242:243], v[122:123], v[250:251]
	s_waitcnt vmcnt(15)
	v_cvt_f32_ubyte0_e32 v240, v18
	v_cvt_f32_ubyte1_e32 v241, v18
	v_cvt_f32_ubyte2_e32 v242, v18
	v_cvt_f32_ubyte3_e32 v243, v18
	v_pk_fma_f32 v[248:249], v[244:245], v[116:117], v[248:249]
	v_pk_fma_f32 v[250:251], v[246:247], v[110:111], v[250:251]
	v_cvt_f32_ubyte0_e32 v244, v19
	v_cvt_f32_ubyte1_e32 v245, v19
	v_cvt_f32_ubyte2_e32 v246, v19
	v_cvt_f32_ubyte3_e32 v247, v19
	v_pk_fma_f32 v[248:249], v[240:241], v[156:157], v[248:249]
	v_pk_fma_f32 v[250:251], v[242:243], v[146:147], v[250:251]
	v_cvt_f32_ubyte0_e32 v240, v20
	v_cvt_f32_ubyte1_e32 v241, v20
	v_cvt_f32_ubyte2_e32 v242, v20
	v_cvt_f32_ubyte3_e32 v243, v20
	v_pk_fma_f32 v[248:249], v[244:245], v[142:143], v[248:249]
	v_pk_fma_f32 v[250:251], v[246:247], v[130:131], v[250:251]
	v_cvt_f32_ubyte0_e32 v244, v21
	v_cvt_f32_ubyte1_e32 v245, v21
	v_cvt_f32_ubyte2_e32 v246, v21
	v_cvt_f32_ubyte3_e32 v247, v21
	global_load_dwordx4 v[18:21], v[194:195], off offset:2048
	v_pk_fma_f32 v[248:249], v[240:241], v[124:125], v[248:249]
	v_pk_fma_f32 v[250:251], v[242:243], v[114:115], v[250:251]
	s_waitcnt vmcnt(15)
	v_cvt_f32_ubyte0_e32 v240, v22
	v_cvt_f32_ubyte1_e32 v241, v22
	v_cvt_f32_ubyte2_e32 v242, v22
	v_cvt_f32_ubyte3_e32 v243, v22
	v_pk_fma_f32 v[248:249], v[244:245], v[108:109], v[248:249]
	v_pk_fma_f32 v[250:251], v[246:247], v[104:105], v[250:251]
	v_cvt_f32_ubyte0_e32 v244, v23
	v_cvt_f32_ubyte1_e32 v245, v23
	v_cvt_f32_ubyte2_e32 v246, v23
	v_cvt_f32_ubyte3_e32 v247, v23
	v_pk_fma_f32 v[248:249], v[240:241], v[154:155], v[248:249]
	v_pk_fma_f32 v[250:251], v[242:243], v[138:139], v[250:251]
	v_cvt_f32_ubyte0_e32 v240, v24
	v_cvt_f32_ubyte1_e32 v241, v24
	v_cvt_f32_ubyte2_e32 v242, v24
	v_cvt_f32_ubyte3_e32 v243, v24
	v_pk_fma_f32 v[248:249], v[244:245], v[150:151], v[248:249]
	v_pk_fma_f32 v[250:251], v[246:247], v[132:133], v[250:251]
	v_cvt_f32_ubyte0_e32 v244, v25
	v_cvt_f32_ubyte1_e32 v245, v25
	v_cvt_f32_ubyte2_e32 v246, v25
	v_cvt_f32_ubyte3_e32 v247, v25
	global_load_dwordx4 v[22:25], v[194:195], off offset:3072
	v_pk_fma_f32 v[248:249], v[240:241], v[144:145], v[248:249]
	v_pk_fma_f32 v[250:251], v[242:243], v[126:127], v[250:251]
	v_readlane_b32 s30, v76, 13
	s_lshl_b32 s30, s30, 12
	v_lshl_add_u64 v[194:195], v[86:87], 0, s[30:31]
	s_waitcnt vmcnt(15)
	v_cvt_f32_ubyte0_e32 v240, v26
	v_cvt_f32_ubyte1_e32 v241, v26
	v_cvt_f32_ubyte2_e32 v242, v26
	v_cvt_f32_ubyte3_e32 v243, v26
	v_pk_fma_f32 v[248:249], v[244:245], v[134:135], v[248:249]
	v_pk_fma_f32 v[250:251], v[246:247], v[118:119], v[250:251]
	v_cvt_f32_ubyte0_e32 v244, v27
	v_cvt_f32_ubyte1_e32 v245, v27
	v_cvt_f32_ubyte2_e32 v246, v27
	v_cvt_f32_ubyte3_e32 v247, v27
	v_pk_add_f32 v[252:253], v[248:249], v[250:251]
	v_pk_mul_f32 v[248:249], v[240:241], v[162:163]
	v_pk_mul_f32 v[250:251], v[242:243], v[160:161]
	v_cvt_f32_ubyte0_e32 v240, v28
	v_cvt_f32_ubyte1_e32 v241, v28
	v_cvt_f32_ubyte2_e32 v242, v28
	v_cvt_f32_ubyte3_e32 v243, v28
	v_pk_fma_f32 v[248:249], v[244:245], v[158:159], v[248:249]
	v_pk_fma_f32 v[250:251], v[246:247], v[148:149], v[250:251]
	v_add_f32_e32 v186, v252, v253
	v_cvt_f32_ubyte0_e32 v244, v29
	v_cvt_f32_ubyte1_e32 v245, v29
	v_cvt_f32_ubyte2_e32 v246, v29
	v_cvt_f32_ubyte3_e32 v247, v29
	global_load_dwordx4 v[26:29], v[194:195], off
	v_pk_fma_f32 v[248:249], v[240:241], v[140:141], v[248:249]
	v_pk_fma_f32 v[250:251], v[242:243], v[128:129], v[250:251]
	s_waitcnt vmcnt(15)
	v_cvt_f32_ubyte0_e32 v240, v30
	v_cvt_f32_ubyte1_e32 v241, v30
	v_cvt_f32_ubyte2_e32 v242, v30
	v_cvt_f32_ubyte3_e32 v243, v30
	v_pk_fma_f32 v[248:249], v[244:245], v[120:121], v[248:249]
	v_pk_fma_f32 v[250:251], v[246:247], v[112:113], v[250:251]
	v_cvt_f32_ubyte0_e32 v244, v31
	v_cvt_f32_ubyte1_e32 v245, v31
	v_cvt_f32_ubyte2_e32 v246, v31
	v_cvt_f32_ubyte3_e32 v247, v31
	v_pk_fma_f32 v[248:249], v[240:241], v[106:107], v[248:249]
	v_pk_fma_f32 v[250:251], v[242:243], v[102:103], v[250:251]
	v_cvt_f32_ubyte0_e32 v240, v32
	v_cvt_f32_ubyte1_e32 v241, v32
	v_cvt_f32_ubyte2_e32 v242, v32
	v_cvt_f32_ubyte3_e32 v243, v32
	v_pk_fma_f32 v[248:249], v[244:245], v[152:153], v[248:249]
	v_pk_fma_f32 v[250:251], v[246:247], v[100:101], v[250:251]
	v_cvt_f32_ubyte0_e32 v244, v33
	v_cvt_f32_ubyte1_e32 v245, v33
	v_cvt_f32_ubyte2_e32 v246, v33
	v_cvt_f32_ubyte3_e32 v247, v33
	global_load_dwordx4 v[30:33], v[194:195], off offset:1024
	v_pk_fma_f32 v[248:249], v[240:241], v[136:137], v[248:249]
	v_pk_fma_f32 v[250:251], v[242:243], v[122:123], v[250:251]
	s_waitcnt vmcnt(15)
	v_cvt_f32_ubyte0_e32 v240, v34
	v_cvt_f32_ubyte1_e32 v241, v34
	v_cvt_f32_ubyte2_e32 v242, v34
	v_cvt_f32_ubyte3_e32 v243, v34
	v_pk_fma_f32 v[248:249], v[244:245], v[116:117], v[248:249]
	v_pk_fma_f32 v[250:251], v[246:247], v[110:111], v[250:251]
	v_cvt_f32_ubyte0_e32 v244, v35
	v_cvt_f32_ubyte1_e32 v245, v35
	v_cvt_f32_ubyte2_e32 v246, v35
	v_cvt_f32_ubyte3_e32 v247, v35
	v_pk_fma_f32 v[248:249], v[240:241], v[156:157], v[248:249]
	v_pk_fma_f32 v[250:251], v[242:243], v[146:147], v[250:251]
	v_cvt_f32_ubyte0_e32 v240, v36
	v_cvt_f32_ubyte1_e32 v241, v36
	v_cvt_f32_ubyte2_e32 v242, v36
	v_cvt_f32_ubyte3_e32 v243, v36
	v_pk_fma_f32 v[248:249], v[244:245], v[142:143], v[248:249]
	v_pk_fma_f32 v[250:251], v[246:247], v[130:131], v[250:251]
	v_cvt_f32_ubyte0_e32 v244, v37
	v_cvt_f32_ubyte1_e32 v245, v37
	v_cvt_f32_ubyte2_e32 v246, v37
	v_cvt_f32_ubyte3_e32 v247, v37
	global_load_dwordx4 v[34:37], v[194:195], off offset:2048
	v_pk_fma_f32 v[248:249], v[240:241], v[124:125], v[248:249]
	v_pk_fma_f32 v[250:251], v[242:243], v[114:115], v[250:251]
	s_waitcnt vmcnt(15)
	v_cvt_f32_ubyte0_e32 v240, v38
	v_cvt_f32_ubyte1_e32 v241, v38
	v_cvt_f32_ubyte2_e32 v242, v38
	v_cvt_f32_ubyte3_e32 v243, v38
	v_pk_fma_f32 v[248:249], v[244:245], v[108:109], v[248:249]
	v_pk_fma_f32 v[250:251], v[246:247], v[104:105], v[250:251]
	v_cvt_f32_ubyte0_e32 v244, v39
	v_cvt_f32_ubyte1_e32 v245, v39
	v_cvt_f32_ubyte2_e32 v246, v39
	v_cvt_f32_ubyte3_e32 v247, v39
	v_pk_fma_f32 v[248:249], v[240:241], v[154:155], v[248:249]
	v_pk_fma_f32 v[250:251], v[242:243], v[138:139], v[250:251]
	v_cvt_f32_ubyte0_e32 v240, v40
	v_cvt_f32_ubyte1_e32 v241, v40
	v_cvt_f32_ubyte2_e32 v242, v40
	v_cvt_f32_ubyte3_e32 v243, v40
	v_pk_fma_f32 v[248:249], v[244:245], v[150:151], v[248:249]
	v_pk_fma_f32 v[250:251], v[246:247], v[132:133], v[250:251]
	v_cvt_f32_ubyte0_e32 v244, v41
	v_cvt_f32_ubyte1_e32 v245, v41
	v_cvt_f32_ubyte2_e32 v246, v41
	v_cvt_f32_ubyte3_e32 v247, v41
	global_load_dwordx4 v[38:41], v[194:195], off offset:3072
	v_pk_fma_f32 v[248:249], v[240:241], v[144:145], v[248:249]
	v_pk_fma_f32 v[250:251], v[242:243], v[126:127], v[250:251]
	v_readlane_b32 s30, v76, 14
	s_lshl_b32 s30, s30, 12
	v_lshl_add_u64 v[194:195], v[86:87], 0, s[30:31]
	s_waitcnt vmcnt(15)
	v_cvt_f32_ubyte0_e32 v240, v42
	v_cvt_f32_ubyte1_e32 v241, v42
	v_cvt_f32_ubyte2_e32 v242, v42
	v_cvt_f32_ubyte3_e32 v243, v42
	v_pk_fma_f32 v[248:249], v[244:245], v[134:135], v[248:249]
	v_pk_fma_f32 v[250:251], v[246:247], v[118:119], v[250:251]
	v_cvt_f32_ubyte0_e32 v244, v43
	v_cvt_f32_ubyte1_e32 v245, v43
	v_cvt_f32_ubyte2_e32 v246, v43
	v_cvt_f32_ubyte3_e32 v247, v43
	v_pk_add_f32 v[252:253], v[248:249], v[250:251]
	v_pk_mul_f32 v[248:249], v[240:241], v[162:163]
	v_pk_mul_f32 v[250:251], v[242:243], v[160:161]
	v_cvt_f32_ubyte0_e32 v240, v44
	v_cvt_f32_ubyte1_e32 v241, v44
	v_cvt_f32_ubyte2_e32 v242, v44
	v_cvt_f32_ubyte3_e32 v243, v44
	v_pk_fma_f32 v[248:249], v[244:245], v[158:159], v[248:249]
	v_pk_fma_f32 v[250:251], v[246:247], v[148:149], v[250:251]
	v_add_f32_e32 v187, v252, v253
	v_cvt_f32_ubyte0_e32 v244, v45
	v_cvt_f32_ubyte1_e32 v245, v45
	v_cvt_f32_ubyte2_e32 v246, v45
	v_cvt_f32_ubyte3_e32 v247, v45
	global_load_dwordx4 v[42:45], v[194:195], off
	v_pk_fma_f32 v[248:249], v[240:241], v[140:141], v[248:249]
	v_pk_fma_f32 v[250:251], v[242:243], v[128:129], v[250:251]
	s_waitcnt vmcnt(15)
	v_cvt_f32_ubyte0_e32 v240, v46
	v_cvt_f32_ubyte1_e32 v241, v46
	v_cvt_f32_ubyte2_e32 v242, v46
	v_cvt_f32_ubyte3_e32 v243, v46
	v_pk_fma_f32 v[248:249], v[244:245], v[120:121], v[248:249]
	v_pk_fma_f32 v[250:251], v[246:247], v[112:113], v[250:251]
	v_cvt_f32_ubyte0_e32 v244, v47
	v_cvt_f32_ubyte1_e32 v245, v47
	v_cvt_f32_ubyte2_e32 v246, v47
	v_cvt_f32_ubyte3_e32 v247, v47
	v_pk_fma_f32 v[248:249], v[240:241], v[106:107], v[248:249]
	v_pk_fma_f32 v[250:251], v[242:243], v[102:103], v[250:251]
	v_cvt_f32_ubyte0_e32 v240, v48
	v_cvt_f32_ubyte1_e32 v241, v48
	v_cvt_f32_ubyte2_e32 v242, v48
	v_cvt_f32_ubyte3_e32 v243, v48
	v_pk_fma_f32 v[248:249], v[244:245], v[152:153], v[248:249]
	v_pk_fma_f32 v[250:251], v[246:247], v[100:101], v[250:251]
	v_cvt_f32_ubyte0_e32 v244, v49
	v_cvt_f32_ubyte1_e32 v245, v49
	v_cvt_f32_ubyte2_e32 v246, v49
	v_cvt_f32_ubyte3_e32 v247, v49
	global_load_dwordx4 v[46:49], v[194:195], off offset:1024
	v_pk_fma_f32 v[248:249], v[240:241], v[136:137], v[248:249]
	v_pk_fma_f32 v[250:251], v[242:243], v[122:123], v[250:251]
	s_waitcnt vmcnt(15)
	v_cvt_f32_ubyte0_e32 v240, v50
	v_cvt_f32_ubyte1_e32 v241, v50
	v_cvt_f32_ubyte2_e32 v242, v50
	v_cvt_f32_ubyte3_e32 v243, v50
	v_pk_fma_f32 v[248:249], v[244:245], v[116:117], v[248:249]
	v_pk_fma_f32 v[250:251], v[246:247], v[110:111], v[250:251]
	v_cvt_f32_ubyte0_e32 v244, v51
	v_cvt_f32_ubyte1_e32 v245, v51
	v_cvt_f32_ubyte2_e32 v246, v51
	v_cvt_f32_ubyte3_e32 v247, v51
	v_pk_fma_f32 v[248:249], v[240:241], v[156:157], v[248:249]
	v_pk_fma_f32 v[250:251], v[242:243], v[146:147], v[250:251]
	v_cvt_f32_ubyte0_e32 v240, v52
	v_cvt_f32_ubyte1_e32 v241, v52
	v_cvt_f32_ubyte2_e32 v242, v52
	v_cvt_f32_ubyte3_e32 v243, v52
	v_pk_fma_f32 v[248:249], v[244:245], v[142:143], v[248:249]
	v_pk_fma_f32 v[250:251], v[246:247], v[130:131], v[250:251]
	v_cvt_f32_ubyte0_e32 v244, v53
	v_cvt_f32_ubyte1_e32 v245, v53
	v_cvt_f32_ubyte2_e32 v246, v53
	v_cvt_f32_ubyte3_e32 v247, v53
	global_load_dwordx4 v[50:53], v[194:195], off offset:2048
	v_pk_fma_f32 v[248:249], v[240:241], v[124:125], v[248:249]
	v_pk_fma_f32 v[250:251], v[242:243], v[114:115], v[250:251]
	s_waitcnt vmcnt(15)
	v_cvt_f32_ubyte0_e32 v240, v54
	v_cvt_f32_ubyte1_e32 v241, v54
	v_cvt_f32_ubyte2_e32 v242, v54
	v_cvt_f32_ubyte3_e32 v243, v54
	v_pk_fma_f32 v[248:249], v[244:245], v[108:109], v[248:249]
	v_pk_fma_f32 v[250:251], v[246:247], v[104:105], v[250:251]
	v_cvt_f32_ubyte0_e32 v244, v55
	v_cvt_f32_ubyte1_e32 v245, v55
	v_cvt_f32_ubyte2_e32 v246, v55
	v_cvt_f32_ubyte3_e32 v247, v55
	v_pk_fma_f32 v[248:249], v[240:241], v[154:155], v[248:249]
	v_pk_fma_f32 v[250:251], v[242:243], v[138:139], v[250:251]
	v_cvt_f32_ubyte0_e32 v240, v56
	v_cvt_f32_ubyte1_e32 v241, v56
	v_cvt_f32_ubyte2_e32 v242, v56
	v_cvt_f32_ubyte3_e32 v243, v56
	v_pk_fma_f32 v[248:249], v[244:245], v[150:151], v[248:249]
	v_pk_fma_f32 v[250:251], v[246:247], v[132:133], v[250:251]
	v_cvt_f32_ubyte0_e32 v244, v57
	v_cvt_f32_ubyte1_e32 v245, v57
	v_cvt_f32_ubyte2_e32 v246, v57
	v_cvt_f32_ubyte3_e32 v247, v57
	global_load_dwordx4 v[54:57], v[194:195], off offset:3072
	v_pk_fma_f32 v[248:249], v[240:241], v[144:145], v[248:249]
	v_pk_fma_f32 v[250:251], v[242:243], v[126:127], v[250:251]
	v_readlane_b32 s30, v76, 15
	s_lshl_b32 s30, s30, 12
	v_lshl_add_u64 v[194:195], v[86:87], 0, s[30:31]
	s_waitcnt vmcnt(15)
	v_cvt_f32_ubyte0_e32 v240, v58
	v_cvt_f32_ubyte1_e32 v241, v58
	v_cvt_f32_ubyte2_e32 v242, v58
	v_cvt_f32_ubyte3_e32 v243, v58
	v_pk_fma_f32 v[248:249], v[244:245], v[134:135], v[248:249]
	v_pk_fma_f32 v[250:251], v[246:247], v[118:119], v[250:251]
	v_cvt_f32_ubyte0_e32 v244, v59
	v_cvt_f32_ubyte1_e32 v245, v59
	v_cvt_f32_ubyte2_e32 v246, v59
	v_cvt_f32_ubyte3_e32 v247, v59
	v_pk_add_f32 v[252:253], v[248:249], v[250:251]
	v_pk_mul_f32 v[248:249], v[240:241], v[162:163]
	v_pk_mul_f32 v[250:251], v[242:243], v[160:161]
	v_cvt_f32_ubyte0_e32 v240, v60
	v_cvt_f32_ubyte1_e32 v241, v60
	v_cvt_f32_ubyte2_e32 v242, v60
	v_cvt_f32_ubyte3_e32 v243, v60
	v_pk_fma_f32 v[248:249], v[244:245], v[158:159], v[248:249]
	v_pk_fma_f32 v[250:251], v[246:247], v[148:149], v[250:251]
	v_add_f32_e32 v188, v252, v253
	v_cvt_f32_ubyte0_e32 v244, v61
	v_cvt_f32_ubyte1_e32 v245, v61
	v_cvt_f32_ubyte2_e32 v246, v61
	v_cvt_f32_ubyte3_e32 v247, v61
	global_load_dwordx4 v[58:61], v[194:195], off
	v_pk_fma_f32 v[248:249], v[240:241], v[140:141], v[248:249]
	v_pk_fma_f32 v[250:251], v[242:243], v[128:129], v[250:251]
	s_waitcnt vmcnt(15)
	v_cvt_f32_ubyte0_e32 v240, v62
	v_cvt_f32_ubyte1_e32 v241, v62
	v_cvt_f32_ubyte2_e32 v242, v62
	v_cvt_f32_ubyte3_e32 v243, v62
	v_pk_fma_f32 v[248:249], v[244:245], v[120:121], v[248:249]
	v_pk_fma_f32 v[250:251], v[246:247], v[112:113], v[250:251]
	v_cvt_f32_ubyte0_e32 v244, v63
	v_cvt_f32_ubyte1_e32 v245, v63
	v_cvt_f32_ubyte2_e32 v246, v63
	v_cvt_f32_ubyte3_e32 v247, v63
	v_pk_fma_f32 v[248:249], v[240:241], v[106:107], v[248:249]
	v_pk_fma_f32 v[250:251], v[242:243], v[102:103], v[250:251]
	v_cvt_f32_ubyte0_e32 v240, v64
	v_cvt_f32_ubyte1_e32 v241, v64
	v_cvt_f32_ubyte2_e32 v242, v64
	v_cvt_f32_ubyte3_e32 v243, v64
	v_pk_fma_f32 v[248:249], v[244:245], v[152:153], v[248:249]
	v_pk_fma_f32 v[250:251], v[246:247], v[100:101], v[250:251]
	v_cvt_f32_ubyte0_e32 v244, v65
	v_cvt_f32_ubyte1_e32 v245, v65
	v_cvt_f32_ubyte2_e32 v246, v65
	v_cvt_f32_ubyte3_e32 v247, v65
	global_load_dwordx4 v[62:65], v[194:195], off offset:1024
	v_pk_fma_f32 v[248:249], v[240:241], v[136:137], v[248:249]
	v_pk_fma_f32 v[250:251], v[242:243], v[122:123], v[250:251]
	s_waitcnt vmcnt(15)
	v_cvt_f32_ubyte0_e32 v240, v66
	v_cvt_f32_ubyte1_e32 v241, v66
	v_cvt_f32_ubyte2_e32 v242, v66
	v_cvt_f32_ubyte3_e32 v243, v66
	v_pk_fma_f32 v[248:249], v[244:245], v[116:117], v[248:249]
	v_pk_fma_f32 v[250:251], v[246:247], v[110:111], v[250:251]
	v_cvt_f32_ubyte0_e32 v244, v67
	v_cvt_f32_ubyte1_e32 v245, v67
	v_cvt_f32_ubyte2_e32 v246, v67
	v_cvt_f32_ubyte3_e32 v247, v67
	v_pk_fma_f32 v[248:249], v[240:241], v[156:157], v[248:249]
	v_pk_fma_f32 v[250:251], v[242:243], v[146:147], v[250:251]
	v_cvt_f32_ubyte0_e32 v240, v68
	v_cvt_f32_ubyte1_e32 v241, v68
	v_cvt_f32_ubyte2_e32 v242, v68
	v_cvt_f32_ubyte3_e32 v243, v68
	v_pk_fma_f32 v[248:249], v[244:245], v[142:143], v[248:249]
	v_pk_fma_f32 v[250:251], v[246:247], v[130:131], v[250:251]
	v_cvt_f32_ubyte0_e32 v244, v69
	v_cvt_f32_ubyte1_e32 v245, v69
	v_cvt_f32_ubyte2_e32 v246, v69
	v_cvt_f32_ubyte3_e32 v247, v69
	global_load_dwordx4 v[66:69], v[194:195], off offset:2048
	v_pk_fma_f32 v[248:249], v[240:241], v[124:125], v[248:249]
	v_pk_fma_f32 v[250:251], v[242:243], v[114:115], v[250:251]
	s_waitcnt vmcnt(15)
	v_cvt_f32_ubyte0_e32 v240, v70
	v_cvt_f32_ubyte1_e32 v241, v70
	v_cvt_f32_ubyte2_e32 v242, v70
	v_cvt_f32_ubyte3_e32 v243, v70
	v_pk_fma_f32 v[248:249], v[244:245], v[108:109], v[248:249]
	v_pk_fma_f32 v[250:251], v[246:247], v[104:105], v[250:251]
	v_cvt_f32_ubyte0_e32 v244, v71
	v_cvt_f32_ubyte1_e32 v245, v71
	v_cvt_f32_ubyte2_e32 v246, v71
	v_cvt_f32_ubyte3_e32 v247, v71
	v_pk_fma_f32 v[248:249], v[240:241], v[154:155], v[248:249]
	v_pk_fma_f32 v[250:251], v[242:243], v[138:139], v[250:251]
	v_cvt_f32_ubyte0_e32 v240, v72
	v_cvt_f32_ubyte1_e32 v241, v72
	v_cvt_f32_ubyte2_e32 v242, v72
	v_cvt_f32_ubyte3_e32 v243, v72
	v_pk_fma_f32 v[248:249], v[244:245], v[150:151], v[248:249]
	v_pk_fma_f32 v[250:251], v[246:247], v[132:133], v[250:251]
	v_cvt_f32_ubyte0_e32 v244, v73
	v_cvt_f32_ubyte1_e32 v245, v73
	v_cvt_f32_ubyte2_e32 v246, v73
	v_cvt_f32_ubyte3_e32 v247, v73
	global_load_dwordx4 v[70:73], v[194:195], off offset:3072
	v_pk_fma_f32 v[248:249], v[240:241], v[144:145], v[248:249]
	v_pk_fma_f32 v[250:251], v[242:243], v[126:127], v[250:251]
	s_waitcnt vmcnt(15)
	v_cvt_f32_ubyte0_e32 v240, v10
	v_cvt_f32_ubyte1_e32 v241, v10
	v_cvt_f32_ubyte2_e32 v242, v10
	v_cvt_f32_ubyte3_e32 v243, v10
	v_pk_fma_f32 v[248:249], v[244:245], v[134:135], v[248:249]
	v_pk_fma_f32 v[250:251], v[246:247], v[118:119], v[250:251]
	v_cvt_f32_ubyte0_e32 v244, v11
	v_cvt_f32_ubyte1_e32 v245, v11
	v_cvt_f32_ubyte2_e32 v246, v11
	v_cvt_f32_ubyte3_e32 v247, v11
	v_pk_add_f32 v[252:253], v[248:249], v[250:251]
	v_pk_mul_f32 v[248:249], v[240:241], v[162:163]
	v_pk_mul_f32 v[250:251], v[242:243], v[160:161]
	v_cvt_f32_ubyte0_e32 v240, v12
	v_cvt_f32_ubyte1_e32 v241, v12
	v_cvt_f32_ubyte2_e32 v242, v12
	v_cvt_f32_ubyte3_e32 v243, v12
	v_pk_fma_f32 v[248:249], v[244:245], v[158:159], v[248:249]
	v_pk_fma_f32 v[250:251], v[246:247], v[148:149], v[250:251]
	v_add_f32_e32 v189, v252, v253
	v_cvt_f32_ubyte0_e32 v244, v13
	v_cvt_f32_ubyte1_e32 v245, v13
	v_cvt_f32_ubyte2_e32 v246, v13
	v_cvt_f32_ubyte3_e32 v247, v13
	v_pk_fma_f32 v[248:249], v[240:241], v[140:141], v[248:249]
	v_pk_fma_f32 v[250:251], v[242:243], v[128:129], v[250:251]
	s_waitcnt vmcnt(14)
	v_cvt_f32_ubyte0_e32 v240, v14
	v_cvt_f32_ubyte1_e32 v241, v14
	v_cvt_f32_ubyte2_e32 v242, v14
	v_cvt_f32_ubyte3_e32 v243, v14
	v_pk_fma_f32 v[248:249], v[244:245], v[120:121], v[248:249]
	v_pk_fma_f32 v[250:251], v[246:247], v[112:113], v[250:251]
	v_cvt_f32_ubyte0_e32 v244, v15
	v_cvt_f32_ubyte1_e32 v245, v15
	v_cvt_f32_ubyte2_e32 v246, v15
	v_cvt_f32_ubyte3_e32 v247, v15
	v_pk_fma_f32 v[248:249], v[240:241], v[106:107], v[248:249]
	v_pk_fma_f32 v[250:251], v[242:243], v[102:103], v[250:251]
	v_cvt_f32_ubyte0_e32 v240, v16
	v_cvt_f32_ubyte1_e32 v241, v16
	v_cvt_f32_ubyte2_e32 v242, v16
	v_cvt_f32_ubyte3_e32 v243, v16
	v_pk_fma_f32 v[248:249], v[244:245], v[152:153], v[248:249]
	v_pk_fma_f32 v[250:251], v[246:247], v[100:101], v[250:251]
	v_cvt_f32_ubyte0_e32 v244, v17
	v_cvt_f32_ubyte1_e32 v245, v17
	v_cvt_f32_ubyte2_e32 v246, v17
	v_cvt_f32_ubyte3_e32 v247, v17
	v_pk_fma_f32 v[248:249], v[240:241], v[136:137], v[248:249]
	v_pk_fma_f32 v[250:251], v[242:243], v[122:123], v[250:251]
	s_waitcnt vmcnt(13)
	v_cvt_f32_ubyte0_e32 v240, v18
	v_cvt_f32_ubyte1_e32 v241, v18
	v_cvt_f32_ubyte2_e32 v242, v18
	v_cvt_f32_ubyte3_e32 v243, v18
	v_pk_fma_f32 v[248:249], v[244:245], v[116:117], v[248:249]
	v_pk_fma_f32 v[250:251], v[246:247], v[110:111], v[250:251]
	v_cvt_f32_ubyte0_e32 v244, v19
	v_cvt_f32_ubyte1_e32 v245, v19
	v_cvt_f32_ubyte2_e32 v246, v19
	v_cvt_f32_ubyte3_e32 v247, v19
	v_pk_fma_f32 v[248:249], v[240:241], v[156:157], v[248:249]
	v_pk_fma_f32 v[250:251], v[242:243], v[146:147], v[250:251]
	v_cvt_f32_ubyte0_e32 v240, v20
	v_cvt_f32_ubyte1_e32 v241, v20
	v_cvt_f32_ubyte2_e32 v242, v20
	v_cvt_f32_ubyte3_e32 v243, v20
	v_pk_fma_f32 v[248:249], v[244:245], v[142:143], v[248:249]
	v_pk_fma_f32 v[250:251], v[246:247], v[130:131], v[250:251]
	v_cvt_f32_ubyte0_e32 v244, v21
	v_cvt_f32_ubyte1_e32 v245, v21
	v_cvt_f32_ubyte2_e32 v246, v21
	v_cvt_f32_ubyte3_e32 v247, v21
	v_pk_fma_f32 v[248:249], v[240:241], v[124:125], v[248:249]
	v_pk_fma_f32 v[250:251], v[242:243], v[114:115], v[250:251]
	s_waitcnt vmcnt(12)
	v_cvt_f32_ubyte0_e32 v240, v22
	v_cvt_f32_ubyte1_e32 v241, v22
	v_cvt_f32_ubyte2_e32 v242, v22
	v_cvt_f32_ubyte3_e32 v243, v22
	v_pk_fma_f32 v[248:249], v[244:245], v[108:109], v[248:249]
	v_pk_fma_f32 v[250:251], v[246:247], v[104:105], v[250:251]
	v_cvt_f32_ubyte0_e32 v244, v23
	v_cvt_f32_ubyte1_e32 v245, v23
	v_cvt_f32_ubyte2_e32 v246, v23
	v_cvt_f32_ubyte3_e32 v247, v23
	v_pk_fma_f32 v[248:249], v[240:241], v[154:155], v[248:249]
	v_pk_fma_f32 v[250:251], v[242:243], v[138:139], v[250:251]
	v_cvt_f32_ubyte0_e32 v240, v24
	v_cvt_f32_ubyte1_e32 v241, v24
	v_cvt_f32_ubyte2_e32 v242, v24
	v_cvt_f32_ubyte3_e32 v243, v24
	v_pk_fma_f32 v[248:249], v[244:245], v[150:151], v[248:249]
	v_pk_fma_f32 v[250:251], v[246:247], v[132:133], v[250:251]
	v_cvt_f32_ubyte0_e32 v244, v25
	v_cvt_f32_ubyte1_e32 v245, v25
	v_cvt_f32_ubyte2_e32 v246, v25
	v_cvt_f32_ubyte3_e32 v247, v25
	v_pk_fma_f32 v[248:249], v[240:241], v[144:145], v[248:249]
	v_pk_fma_f32 v[250:251], v[242:243], v[126:127], v[250:251]
	s_waitcnt vmcnt(11)
	v_cvt_f32_ubyte0_e32 v240, v26
	v_cvt_f32_ubyte1_e32 v241, v26
	v_cvt_f32_ubyte2_e32 v242, v26
	v_cvt_f32_ubyte3_e32 v243, v26
	v_pk_fma_f32 v[248:249], v[244:245], v[134:135], v[248:249]
	v_pk_fma_f32 v[250:251], v[246:247], v[118:119], v[250:251]
	v_cvt_f32_ubyte0_e32 v244, v27
	v_cvt_f32_ubyte1_e32 v245, v27
	v_cvt_f32_ubyte2_e32 v246, v27
	v_cvt_f32_ubyte3_e32 v247, v27
	v_pk_add_f32 v[252:253], v[248:249], v[250:251]
	v_pk_mul_f32 v[248:249], v[240:241], v[162:163]
	v_pk_mul_f32 v[250:251], v[242:243], v[160:161]
	v_cvt_f32_ubyte0_e32 v240, v28
	v_cvt_f32_ubyte1_e32 v241, v28
	v_cvt_f32_ubyte2_e32 v242, v28
	v_cvt_f32_ubyte3_e32 v243, v28
	v_pk_fma_f32 v[248:249], v[244:245], v[158:159], v[248:249]
	v_pk_fma_f32 v[250:251], v[246:247], v[148:149], v[250:251]
	v_add_f32_e32 v190, v252, v253
	v_cvt_f32_ubyte0_e32 v244, v29
	v_cvt_f32_ubyte1_e32 v245, v29
	v_cvt_f32_ubyte2_e32 v246, v29
	v_cvt_f32_ubyte3_e32 v247, v29
	v_pk_fma_f32 v[248:249], v[240:241], v[140:141], v[248:249]
	v_pk_fma_f32 v[250:251], v[242:243], v[128:129], v[250:251]
	s_waitcnt vmcnt(10)
	v_cvt_f32_ubyte0_e32 v240, v30
	v_cvt_f32_ubyte1_e32 v241, v30
	v_cvt_f32_ubyte2_e32 v242, v30
	v_cvt_f32_ubyte3_e32 v243, v30
	v_pk_fma_f32 v[248:249], v[244:245], v[120:121], v[248:249]
	v_pk_fma_f32 v[250:251], v[246:247], v[112:113], v[250:251]
	v_cvt_f32_ubyte0_e32 v244, v31
	v_cvt_f32_ubyte1_e32 v245, v31
	v_cvt_f32_ubyte2_e32 v246, v31
	v_cvt_f32_ubyte3_e32 v247, v31
	v_pk_fma_f32 v[248:249], v[240:241], v[106:107], v[248:249]
	v_pk_fma_f32 v[250:251], v[242:243], v[102:103], v[250:251]
	v_cvt_f32_ubyte0_e32 v240, v32
	v_cvt_f32_ubyte1_e32 v241, v32
	v_cvt_f32_ubyte2_e32 v242, v32
	v_cvt_f32_ubyte3_e32 v243, v32
	v_pk_fma_f32 v[248:249], v[244:245], v[152:153], v[248:249]
	v_pk_fma_f32 v[250:251], v[246:247], v[100:101], v[250:251]
	v_cvt_f32_ubyte0_e32 v244, v33
	v_cvt_f32_ubyte1_e32 v245, v33
	v_cvt_f32_ubyte2_e32 v246, v33
	v_cvt_f32_ubyte3_e32 v247, v33
	v_pk_fma_f32 v[248:249], v[240:241], v[136:137], v[248:249]
	v_pk_fma_f32 v[250:251], v[242:243], v[122:123], v[250:251]
	s_waitcnt vmcnt(9)
	v_cvt_f32_ubyte0_e32 v240, v34
	v_cvt_f32_ubyte1_e32 v241, v34
	v_cvt_f32_ubyte2_e32 v242, v34
	v_cvt_f32_ubyte3_e32 v243, v34
	v_pk_fma_f32 v[248:249], v[244:245], v[116:117], v[248:249]
	v_pk_fma_f32 v[250:251], v[246:247], v[110:111], v[250:251]
	v_cvt_f32_ubyte0_e32 v244, v35
	v_cvt_f32_ubyte1_e32 v245, v35
	v_cvt_f32_ubyte2_e32 v246, v35
	v_cvt_f32_ubyte3_e32 v247, v35
	v_pk_fma_f32 v[248:249], v[240:241], v[156:157], v[248:249]
	v_pk_fma_f32 v[250:251], v[242:243], v[146:147], v[250:251]
	v_cvt_f32_ubyte0_e32 v240, v36
	v_cvt_f32_ubyte1_e32 v241, v36
	v_cvt_f32_ubyte2_e32 v242, v36
	v_cvt_f32_ubyte3_e32 v243, v36
	v_pk_fma_f32 v[248:249], v[244:245], v[142:143], v[248:249]
	v_pk_fma_f32 v[250:251], v[246:247], v[130:131], v[250:251]
	v_cvt_f32_ubyte0_e32 v244, v37
	v_cvt_f32_ubyte1_e32 v245, v37
	v_cvt_f32_ubyte2_e32 v246, v37
	v_cvt_f32_ubyte3_e32 v247, v37
	v_pk_fma_f32 v[248:249], v[240:241], v[124:125], v[248:249]
	v_pk_fma_f32 v[250:251], v[242:243], v[114:115], v[250:251]
	s_waitcnt vmcnt(8)
	v_cvt_f32_ubyte0_e32 v240, v38
	v_cvt_f32_ubyte1_e32 v241, v38
	v_cvt_f32_ubyte2_e32 v242, v38
	v_cvt_f32_ubyte3_e32 v243, v38
	v_pk_fma_f32 v[248:249], v[244:245], v[108:109], v[248:249]
	v_pk_fma_f32 v[250:251], v[246:247], v[104:105], v[250:251]
	v_cvt_f32_ubyte0_e32 v244, v39
	v_cvt_f32_ubyte1_e32 v245, v39
	v_cvt_f32_ubyte2_e32 v246, v39
	v_cvt_f32_ubyte3_e32 v247, v39
	v_pk_fma_f32 v[248:249], v[240:241], v[154:155], v[248:249]
	v_pk_fma_f32 v[250:251], v[242:243], v[138:139], v[250:251]
	v_cvt_f32_ubyte0_e32 v240, v40
	v_cvt_f32_ubyte1_e32 v241, v40
	v_cvt_f32_ubyte2_e32 v242, v40
	v_cvt_f32_ubyte3_e32 v243, v40
	v_pk_fma_f32 v[248:249], v[244:245], v[150:151], v[248:249]
	v_pk_fma_f32 v[250:251], v[246:247], v[132:133], v[250:251]
	v_cvt_f32_ubyte0_e32 v244, v41
	v_cvt_f32_ubyte1_e32 v245, v41
	v_cvt_f32_ubyte2_e32 v246, v41
	v_cvt_f32_ubyte3_e32 v247, v41
	v_pk_fma_f32 v[248:249], v[240:241], v[144:145], v[248:249]
	v_pk_fma_f32 v[250:251], v[242:243], v[126:127], v[250:251]
	s_waitcnt vmcnt(7)
	v_cvt_f32_ubyte0_e32 v240, v42
	v_cvt_f32_ubyte1_e32 v241, v42
	v_cvt_f32_ubyte2_e32 v242, v42
	v_cvt_f32_ubyte3_e32 v243, v42
	v_pk_fma_f32 v[248:249], v[244:245], v[134:135], v[248:249]
	v_pk_fma_f32 v[250:251], v[246:247], v[118:119], v[250:251]
	v_cvt_f32_ubyte0_e32 v244, v43
	v_cvt_f32_ubyte1_e32 v245, v43
	v_cvt_f32_ubyte2_e32 v246, v43
	v_cvt_f32_ubyte3_e32 v247, v43
	v_pk_add_f32 v[252:253], v[248:249], v[250:251]
	v_pk_mul_f32 v[248:249], v[240:241], v[162:163]
	v_pk_mul_f32 v[250:251], v[242:243], v[160:161]
	v_cvt_f32_ubyte0_e32 v240, v44
	v_cvt_f32_ubyte1_e32 v241, v44
	v_cvt_f32_ubyte2_e32 v242, v44
	v_cvt_f32_ubyte3_e32 v243, v44
	v_pk_fma_f32 v[248:249], v[244:245], v[158:159], v[248:249]
	v_pk_fma_f32 v[250:251], v[246:247], v[148:149], v[250:251]
	v_add_f32_e32 v191, v252, v253
	v_cvt_f32_ubyte0_e32 v244, v45
	v_cvt_f32_ubyte1_e32 v245, v45
	v_cvt_f32_ubyte2_e32 v246, v45
	v_cvt_f32_ubyte3_e32 v247, v45
	v_pk_fma_f32 v[248:249], v[240:241], v[140:141], v[248:249]
	v_pk_fma_f32 v[250:251], v[242:243], v[128:129], v[250:251]
	s_waitcnt vmcnt(6)
	v_cvt_f32_ubyte0_e32 v240, v46
	v_cvt_f32_ubyte1_e32 v241, v46
	v_cvt_f32_ubyte2_e32 v242, v46
	v_cvt_f32_ubyte3_e32 v243, v46
	v_pk_fma_f32 v[248:249], v[244:245], v[120:121], v[248:249]
	v_pk_fma_f32 v[250:251], v[246:247], v[112:113], v[250:251]
	v_cvt_f32_ubyte0_e32 v244, v47
	v_cvt_f32_ubyte1_e32 v245, v47
	v_cvt_f32_ubyte2_e32 v246, v47
	v_cvt_f32_ubyte3_e32 v247, v47
	v_pk_fma_f32 v[248:249], v[240:241], v[106:107], v[248:249]
	v_pk_fma_f32 v[250:251], v[242:243], v[102:103], v[250:251]
	v_cvt_f32_ubyte0_e32 v240, v48
	v_cvt_f32_ubyte1_e32 v241, v48
	v_cvt_f32_ubyte2_e32 v242, v48
	v_cvt_f32_ubyte3_e32 v243, v48
	v_pk_fma_f32 v[248:249], v[244:245], v[152:153], v[248:249]
	v_pk_fma_f32 v[250:251], v[246:247], v[100:101], v[250:251]
	v_cvt_f32_ubyte0_e32 v244, v49
	v_cvt_f32_ubyte1_e32 v245, v49
	v_cvt_f32_ubyte2_e32 v246, v49
	v_cvt_f32_ubyte3_e32 v247, v49
	v_pk_fma_f32 v[248:249], v[240:241], v[136:137], v[248:249]
	v_pk_fma_f32 v[250:251], v[242:243], v[122:123], v[250:251]
	s_waitcnt vmcnt(5)
	v_cvt_f32_ubyte0_e32 v240, v50
	v_cvt_f32_ubyte1_e32 v241, v50
	v_cvt_f32_ubyte2_e32 v242, v50
	v_cvt_f32_ubyte3_e32 v243, v50
	v_pk_fma_f32 v[248:249], v[244:245], v[116:117], v[248:249]
	v_pk_fma_f32 v[250:251], v[246:247], v[110:111], v[250:251]
	v_cvt_f32_ubyte0_e32 v244, v51
	v_cvt_f32_ubyte1_e32 v245, v51
	v_cvt_f32_ubyte2_e32 v246, v51
	v_cvt_f32_ubyte3_e32 v247, v51
	v_pk_fma_f32 v[248:249], v[240:241], v[156:157], v[248:249]
	v_pk_fma_f32 v[250:251], v[242:243], v[146:147], v[250:251]
	v_cvt_f32_ubyte0_e32 v240, v52
	v_cvt_f32_ubyte1_e32 v241, v52
	v_cvt_f32_ubyte2_e32 v242, v52
	v_cvt_f32_ubyte3_e32 v243, v52
	v_pk_fma_f32 v[248:249], v[244:245], v[142:143], v[248:249]
	v_pk_fma_f32 v[250:251], v[246:247], v[130:131], v[250:251]
	v_cvt_f32_ubyte0_e32 v244, v53
	v_cvt_f32_ubyte1_e32 v245, v53
	v_cvt_f32_ubyte2_e32 v246, v53
	v_cvt_f32_ubyte3_e32 v247, v53
	v_pk_fma_f32 v[248:249], v[240:241], v[124:125], v[248:249]
	v_pk_fma_f32 v[250:251], v[242:243], v[114:115], v[250:251]
	s_waitcnt vmcnt(4)
	v_cvt_f32_ubyte0_e32 v240, v54
	v_cvt_f32_ubyte1_e32 v241, v54
	v_cvt_f32_ubyte2_e32 v242, v54
	v_cvt_f32_ubyte3_e32 v243, v54
	v_pk_fma_f32 v[248:249], v[244:245], v[108:109], v[248:249]
	v_pk_fma_f32 v[250:251], v[246:247], v[104:105], v[250:251]
	v_cvt_f32_ubyte0_e32 v244, v55
	v_cvt_f32_ubyte1_e32 v245, v55
	v_cvt_f32_ubyte2_e32 v246, v55
	v_cvt_f32_ubyte3_e32 v247, v55
	v_pk_fma_f32 v[248:249], v[240:241], v[154:155], v[248:249]
	v_pk_fma_f32 v[250:251], v[242:243], v[138:139], v[250:251]
	v_cvt_f32_ubyte0_e32 v240, v56
	v_cvt_f32_ubyte1_e32 v241, v56
	v_cvt_f32_ubyte2_e32 v242, v56
	v_cvt_f32_ubyte3_e32 v243, v56
	v_pk_fma_f32 v[248:249], v[244:245], v[150:151], v[248:249]
	v_pk_fma_f32 v[250:251], v[246:247], v[132:133], v[250:251]
	v_cvt_f32_ubyte0_e32 v244, v57
	v_cvt_f32_ubyte1_e32 v245, v57
	v_cvt_f32_ubyte2_e32 v246, v57
	v_cvt_f32_ubyte3_e32 v247, v57
	v_pk_fma_f32 v[248:249], v[240:241], v[144:145], v[248:249]
	v_pk_fma_f32 v[250:251], v[242:243], v[126:127], v[250:251]
	s_waitcnt vmcnt(3)
	v_cvt_f32_ubyte0_e32 v240, v58
	v_cvt_f32_ubyte1_e32 v241, v58
	v_cvt_f32_ubyte2_e32 v242, v58
	v_cvt_f32_ubyte3_e32 v243, v58
	v_pk_fma_f32 v[248:249], v[244:245], v[134:135], v[248:249]
	v_pk_fma_f32 v[250:251], v[246:247], v[118:119], v[250:251]
	v_cvt_f32_ubyte0_e32 v244, v59
	v_cvt_f32_ubyte1_e32 v245, v59
	v_cvt_f32_ubyte2_e32 v246, v59
	v_cvt_f32_ubyte3_e32 v247, v59
	v_pk_add_f32 v[252:253], v[248:249], v[250:251]
	v_pk_mul_f32 v[248:249], v[240:241], v[162:163]
	v_pk_mul_f32 v[250:251], v[242:243], v[160:161]
	v_cvt_f32_ubyte0_e32 v240, v60
	v_cvt_f32_ubyte1_e32 v241, v60
	v_cvt_f32_ubyte2_e32 v242, v60
	v_cvt_f32_ubyte3_e32 v243, v60
	v_pk_fma_f32 v[248:249], v[244:245], v[158:159], v[248:249]
	v_pk_fma_f32 v[250:251], v[246:247], v[148:149], v[250:251]
	v_add_f32_e32 v192, v252, v253
	v_cvt_f32_ubyte0_e32 v244, v61
	v_cvt_f32_ubyte1_e32 v245, v61
	v_cvt_f32_ubyte2_e32 v246, v61
	v_cvt_f32_ubyte3_e32 v247, v61
	v_pk_fma_f32 v[248:249], v[240:241], v[140:141], v[248:249]
	v_pk_fma_f32 v[250:251], v[242:243], v[128:129], v[250:251]
	s_waitcnt vmcnt(2)
	v_cvt_f32_ubyte0_e32 v240, v62
	v_cvt_f32_ubyte1_e32 v241, v62
	v_cvt_f32_ubyte2_e32 v242, v62
	v_cvt_f32_ubyte3_e32 v243, v62
	v_pk_fma_f32 v[248:249], v[244:245], v[120:121], v[248:249]
	v_pk_fma_f32 v[250:251], v[246:247], v[112:113], v[250:251]
	v_cvt_f32_ubyte0_e32 v244, v63
	v_cvt_f32_ubyte1_e32 v245, v63
	v_cvt_f32_ubyte2_e32 v246, v63
	v_cvt_f32_ubyte3_e32 v247, v63
	v_pk_fma_f32 v[248:249], v[240:241], v[106:107], v[248:249]
	v_pk_fma_f32 v[250:251], v[242:243], v[102:103], v[250:251]
	v_cvt_f32_ubyte0_e32 v240, v64
	v_cvt_f32_ubyte1_e32 v241, v64
	v_cvt_f32_ubyte2_e32 v242, v64
	v_cvt_f32_ubyte3_e32 v243, v64
	v_pk_fma_f32 v[248:249], v[244:245], v[152:153], v[248:249]
	v_pk_fma_f32 v[250:251], v[246:247], v[100:101], v[250:251]
	v_cvt_f32_ubyte0_e32 v244, v65
	v_cvt_f32_ubyte1_e32 v245, v65
	v_cvt_f32_ubyte2_e32 v246, v65
	v_cvt_f32_ubyte3_e32 v247, v65
	v_pk_fma_f32 v[248:249], v[240:241], v[136:137], v[248:249]
	v_pk_fma_f32 v[250:251], v[242:243], v[122:123], v[250:251]
	s_waitcnt vmcnt(1)
	v_cvt_f32_ubyte0_e32 v240, v66
	v_cvt_f32_ubyte1_e32 v241, v66
	v_cvt_f32_ubyte2_e32 v242, v66
	v_cvt_f32_ubyte3_e32 v243, v66
	v_pk_fma_f32 v[248:249], v[244:245], v[116:117], v[248:249]
	v_pk_fma_f32 v[250:251], v[246:247], v[110:111], v[250:251]
	v_cvt_f32_ubyte0_e32 v244, v67
	v_cvt_f32_ubyte1_e32 v245, v67
	v_cvt_f32_ubyte2_e32 v246, v67
	v_cvt_f32_ubyte3_e32 v247, v67
	v_pk_fma_f32 v[248:249], v[240:241], v[156:157], v[248:249]
	v_pk_fma_f32 v[250:251], v[242:243], v[146:147], v[250:251]
	v_cvt_f32_ubyte0_e32 v240, v68
	v_cvt_f32_ubyte1_e32 v241, v68
	v_cvt_f32_ubyte2_e32 v242, v68
	v_cvt_f32_ubyte3_e32 v243, v68
	v_pk_fma_f32 v[248:249], v[244:245], v[142:143], v[248:249]
	v_pk_fma_f32 v[250:251], v[246:247], v[130:131], v[250:251]
	v_cvt_f32_ubyte0_e32 v244, v69
	v_cvt_f32_ubyte1_e32 v245, v69
	v_cvt_f32_ubyte2_e32 v246, v69
	v_cvt_f32_ubyte3_e32 v247, v69
	v_pk_fma_f32 v[248:249], v[240:241], v[124:125], v[248:249]
	v_pk_fma_f32 v[250:251], v[242:243], v[114:115], v[250:251]
	s_waitcnt vmcnt(0)
	v_cvt_f32_ubyte0_e32 v240, v70
	v_cvt_f32_ubyte1_e32 v241, v70
	v_cvt_f32_ubyte2_e32 v242, v70
	v_cvt_f32_ubyte3_e32 v243, v70
	v_pk_fma_f32 v[248:249], v[244:245], v[108:109], v[248:249]
	v_pk_fma_f32 v[250:251], v[246:247], v[104:105], v[250:251]
	v_cvt_f32_ubyte0_e32 v244, v71
	v_cvt_f32_ubyte1_e32 v245, v71
	v_cvt_f32_ubyte2_e32 v246, v71
	v_cvt_f32_ubyte3_e32 v247, v71
	v_pk_fma_f32 v[248:249], v[240:241], v[154:155], v[248:249]
	v_pk_fma_f32 v[250:251], v[242:243], v[138:139], v[250:251]
	v_cvt_f32_ubyte0_e32 v240, v72
	v_cvt_f32_ubyte1_e32 v241, v72
	v_cvt_f32_ubyte2_e32 v242, v72
	v_cvt_f32_ubyte3_e32 v243, v72
	v_pk_fma_f32 v[248:249], v[244:245], v[150:151], v[248:249]
	v_pk_fma_f32 v[250:251], v[246:247], v[132:133], v[250:251]
	v_cvt_f32_ubyte0_e32 v244, v73
	v_cvt_f32_ubyte1_e32 v245, v73
	v_cvt_f32_ubyte2_e32 v246, v73
	v_cvt_f32_ubyte3_e32 v247, v73
	v_pk_fma_f32 v[248:249], v[240:241], v[144:145], v[248:249]
	v_pk_fma_f32 v[250:251], v[242:243], v[126:127], v[250:251]
	v_pk_fma_f32 v[248:249], v[244:245], v[134:135], v[248:249]
	v_pk_fma_f32 v[250:251], v[246:247], v[118:119], v[250:251]
	v_pk_add_f32 v[252:253], v[248:249], v[250:251]
	v_mov_b32_e32 v14, v190
	v_mov_b32_e32 v15, v191
	v_mov_b32_e32 v16, v192
	v_add_f32_e32 v10, v252, v253
	v_cndmask_b32_e64 v12, v178, v186, s[4:5]
	ds_bpermute_b32 v12, v170, v12
	v_cndmask_b32_e64 v13, v179, v187, s[4:5]
	ds_bpermute_b32 v13, v170, v13
	v_cndmask_b32_e64 v17, v180, v188, s[4:5]
	ds_bpermute_b32 v17, v170, v17
	v_cndmask_b32_e64 v18, v181, v189, s[4:5]
	v_cndmask_b32_e64 v19, v182, v14, s[4:5]
	ds_bpermute_b32 v18, v170, v18
	ds_bpermute_b32 v19, v170, v19
	v_cndmask_b32_e64 v11, v186, v178, s[4:5]
	s_waitcnt lgkmcnt(4)
	v_add_f32_e32 v11, v11, v12
	v_cndmask_b32_e64 v12, v187, v179, s[4:5]
	s_waitcnt lgkmcnt(3)
	v_add_f32_e32 v12, v12, v13
	v_cndmask_b32_e64 v13, v188, v180, s[4:5]
	s_waitcnt lgkmcnt(2)
	v_add_f32_e32 v13, v13, v17
	v_cndmask_b32_e64 v17, v189, v181, s[4:5]
	v_cndmask_b32_e64 v14, v14, v182, s[4:5]
	v_cndmask_b32_e64 v20, v183, v15, s[4:5]
	s_waitcnt lgkmcnt(1)
	v_add_f32_e32 v17, v17, v18
	s_waitcnt lgkmcnt(0)
	v_add_f32_e32 v14, v14, v19
	v_cndmask_b32_e64 v18, v16, v184, s[4:5]
	v_cndmask_b32_e64 v16, v184, v16, s[4:5]
	v_cndmask_b32_e64 v19, v185, v10, s[4:5]
	ds_bpermute_b32 v20, v170, v20
	ds_bpermute_b32 v16, v170, v16
	ds_bpermute_b32 v19, v170, v19
	v_cndmask_b32_e64 v15, v15, v183, s[4:5]
	v_cndmask_b32_e64 v10, v10, v185, s[4:5]
	s_waitcnt lgkmcnt(2)
	v_add_f32_e32 v15, v15, v20
	s_waitcnt lgkmcnt(1)
	v_add_f32_e32 v16, v18, v16
	s_waitcnt lgkmcnt(0)
	v_add_f32_e32 v10, v10, v19
	v_cndmask_b32_e64 v20, v11, v14, s[6:7]
	v_cndmask_b32_e64 v11, v14, v11, s[6:7]
	v_cndmask_b32_e64 v14, v15, v12, s[6:7]
	v_cndmask_b32_e64 v12, v12, v15, s[6:7]
	v_cndmask_b32_e64 v15, v13, v16, s[6:7]
	v_cndmask_b32_e64 v18, v17, v10, s[6:7]
	ds_bpermute_b32 v20, v169, v20
	ds_bpermute_b32 v12, v169, v12
	ds_bpermute_b32 v15, v169, v15
	ds_bpermute_b32 v18, v169, v18
	v_cndmask_b32_e64 v13, v16, v13, s[6:7]
	v_cndmask_b32_e64 v10, v10, v17, s[6:7]
	s_waitcnt lgkmcnt(3)
	v_add_f32_e32 v11, v11, v20
	s_waitcnt lgkmcnt(2)
	v_add_f32_e32 v12, v14, v12
	s_waitcnt lgkmcnt(1)
	v_add_f32_e32 v13, v13, v15
	s_waitcnt lgkmcnt(0)
	v_add_f32_e32 v10, v10, v18
	v_cndmask_b32_e64 v14, v11, v13, s[8:9]
	v_cndmask_b32_e64 v15, v12, v10, s[8:9]
	ds_bpermute_b32 v14, v168, v14
	ds_bpermute_b32 v15, v168, v15
	v_cndmask_b32_e64 v11, v13, v11, s[8:9]
	v_cndmask_b32_e64 v10, v10, v12, s[8:9]
	s_waitcnt lgkmcnt(1)
	v_add_f32_e32 v11, v11, v14
	s_waitcnt lgkmcnt(0)
	v_add_f32_e32 v10, v10, v15
	v_cndmask_b32_e64 v12, v11, v10, s[10:11]
	ds_bpermute_b32 v12, v167, v12
	v_cndmask_b32_e64 v10, v10, v11, s[10:11]
	s_waitcnt lgkmcnt(0)
	v_add_f32_e32 v10, v10, v12
	ds_bpermute_b32 v11, v166, v10
	s_waitcnt lgkmcnt(0)
	v_add_f32_e32 v10, v10, v11
	ds_bpermute_b32 v11, v165, v10
	s_waitcnt lgkmcnt(0)
	v_add_f32_e32 v10, v10, v11
	ds_bpermute_b32 v11, v80, v10
	v_mov_b32_e32 v10, 0
	s_and_saveexec_b64 s[30:31], s[2:3]
	s_cbranch_execz .LBB0_1479
	v_add_f32_e32 v99, v99, v177
	v_pk_mul_f32 v[12:13], v[98:99], v[96:97]
	s_waitcnt lgkmcnt(0)
	v_sub_f32_e32 v10, v11, v13
	v_mul_f32_e32 v10, v12, v10
	v_mul_f32_e32 v11, 0x3f3504f3, v10
	v_cmp_nlt_f32_e64 s[34:35], |v11|, 1.0
	s_and_saveexec_b64 s[52:53], s[34:35]
	s_xor_b64 s[34:35], exec, s[52:53]
	s_cbranch_execz .LBB0_1476
	v_fma_f32 v12, |v11|, s41, v175
	v_fma_f32 v12, |v11|, v12, s42
	v_fma_f32 v12, |v11|, v12, s43
	v_fma_f32 v12, |v11|, v12, s44
	v_fma_f32 v12, |v11|, v12, s45
	v_fma_f32 v12, |v11|, v12, s46
	v_fma_f32 v12, |v11|, v12, |v11|
	v_mul_f32_e32 v13, 0xbfb8aa3b, v12
	v_fma_f32 v14, v12, s47, -v13
	v_rndne_f32_e32 v15, v13
	v_fmac_f32_e32 v14, 0xb2a5705f, v12
	v_sub_f32_e32 v13, v13, v15
	v_add_f32_e32 v13, v13, v14
	v_cvt_i32_f32_e32 v14, v15
	v_exp_f32_e32 v13, v13
	v_cmp_nlt_f32_e32 vcc, s48, v12
	v_ldexp_f32 v13, v13, v14
	s_nop 0
	v_cndmask_b32_e32 v13, 0, v13, vcc
	v_cmp_ngt_f32_e32 vcc, s49, v12
	s_nop 1
	v_cndmask_b32_e32 v12, v176, v13, vcc
	v_sub_f32_e32 v12, 1.0, v12

	.amdhsa_kernel _Z6mk_fwd4Args
		.amdhsa_group_segment_fixed_size 0
		.amdhsa_private_segment_fixed_size 0
		.amdhsa_kernarg_size 472
		.amdhsa_user_sgpr_count 2
		.amdhsa_user_sgpr_dispatch_ptr 0
		.amdhsa_user_sgpr_queue_ptr 0
		.amdhsa_user_sgpr_kernarg_segment_ptr 1
		.amdhsa_user_sgpr_dispatch_id 0
		.amdhsa_user_sgpr_kernarg_preload_length 0
		.amdhsa_user_sgpr_kernarg_preload_offset 0
		.amdhsa_user_sgpr_private_segment_size 0
		.amdhsa_uses_dynamic_stack 0
		.amdhsa_enable_private_segment 0
		.amdhsa_system_sgpr_workgroup_id_x 1
		.amdhsa_system_sgpr_workgroup_id_y 0
		.amdhsa_system_sgpr_workgroup_id_z 0
		.amdhsa_system_sgpr_workgroup_info 0
		.amdhsa_system_vgpr_workitem_id 0
		.amdhsa_next_free_vgpr 256
		.amdhsa_next_free_sgpr 98
		.amdhsa_accum_offset 256
		.amdhsa_reserve_vcc 1
		.amdhsa_float_round_mode_32 0
		.amdhsa_float_round_mode_16_64 0
		.amdhsa_float_denorm_mode_32 3
		.amdhsa_float_denorm_mode_16_64 3
		.amdhsa_dx10_clamp 1
		.amdhsa_ieee_mode 1
		.amdhsa_fp16_overflow 0
		.amdhsa_tg_split 0
		.amdhsa_exception_fp_ieee_invalid_op 0
		.amdhsa_exception_fp_denorm_src 0
		.amdhsa_exception_fp_ieee_div_zero 0
		.amdhsa_exception_fp_ieee_overflow 0
		.amdhsa_exception_fp_ieee_underflow 0
		.amdhsa_exception_fp_ieee_inexact 0
		.amdhsa_exception_int_div_zero 0
	.end_amdhsa_kernel

amdhsa.kernels:
  - .agpr_count:     0
    .args:
      - .offset:         0
        .size:           216
        .value_kind:     by_value
      - .offset:         216
        .size:           4
        .value_kind:     hidden_block_count_x
      - .offset:         220
        .size:           4
        .value_kind:     hidden_block_count_y
      - .offset:         224
        .size:           4
        .value_kind:     hidden_block_count_z
      - .offset:         228
        .size:           2
        .value_kind:     hidden_group_size_x
      - .offset:         230
        .size:           2
        .value_kind:     hidden_group_size_y
      - .offset:         232
        .size:           2
        .value_kind:     hidden_group_size_z
      - .offset:         234
        .size:           2
        .value_kind:     hidden_remainder_x
      - .offset:         236
        .size:           2
        .value_kind:     hidden_remainder_y
      - .offset:         238
        .size:           2
        .value_kind:     hidden_remainder_z
      - .offset:         256
        .size:           8
        .value_kind:     hidden_global_offset_x
      - .offset:         264
        .size:           8
        .value_kind:     hidden_global_offset_y
      - .offset:         272
        .size:           8
        .value_kind:     hidden_global_offset_z
      - .offset:         280
        .size:           2
        .value_kind:     hidden_grid_dims
      - .offset:         336
        .size:           4
        .value_kind:     hidden_dynamic_lds_size
    .group_segment_fixed_size: 0
    .kernarg_segment_align: 8
    .kernarg_segment_size: 472
    .language:       OpenCL C
    .language_version:
      - 2
      - 0
    .max_flat_workgroup_size: 512
    .name:           _Z6mk_fwd4Args
    .private_segment_fixed_size: 0
    .sgpr_count:     104
    .sgpr_spill_count: 241
    .symbol:         _Z6mk_fwd4Args.kd
    .uniform_work_group_size: 1
    .uses_dynamic_stack: false
    .vgpr_count:     256
    .vgpr_spill_count: 0
    .wavefront_size: 64
